# hand-written scan+counting sort+register fp64 accumulation gather, D=24 rows in flight, nt loads
# baseline (speedup 1.0000x reference)
_Z7vq_mainPKfPKiS0_PfPhPdPi:
	s_load_dwordx4 s[4:7], s[0:1], 0x0
	s_load_dwordx2 s[22:23], s[0:1], 0x10
	s_load_dwordx2 s[20:21], s[0:1], 0x18
	s_load_dwordx4 s[12:15], s[0:1], 0x20
	s_load_dwordx2 s[10:11], s[0:1], 0x30
	s_and_b32 s3, s2, 7
	s_lshl_b32 s3, s3, 6
	s_lshr_b32 s16, s2, 3
	s_add_i32 s16, s16, s3
	s_lshr_b32 s18, s16, 5
	s_mov_b32 s19, 0
	s_and_b32 s28, s16, 31
	s_lshl_b32 s28, s28, 4
	s_add_i32 s29, s28, 1
	v_readfirstlane_b32 s17, v0
	v_and_b32_e32 v1, 63, v0
	v_lshlrev_b32_e32 v66, 4, v0
	s_lshr_b32 s17, s17, 6
	s_lshl_b32 s24, s17, 4
	s_lshl_b32 s30, s18, 15
	s_lshl_b32 s31, s18, 23
	v_add_u32_e32 v67, 0x1000, v66
	v_add_u32_e32 v68, 0x2000, v66
	v_add_u32_e32 v69, 0x3000, v66
	v_add_u32_e32 v70, 0x4000, v66
	v_add_u32_e32 v71, 0x5000, v66
	v_add_u32_e32 v72, 0x6000, v66
	v_add_u32_e32 v73, 0x7000, v66
	s_waitcnt lgkmcnt(0)
	s_add_u32 s34, s6, s30
	s_addc_u32 s35, s7, 0
	s_add_u32 s32, s4, s31
	s_addc_u32 s33, s5, 0
	global_load_dwordx4 v[74:77], v66, s[34:35]
	global_load_dwordx4 v[78:81], v67, s[34:35]
	global_load_dwordx4 v[82:85], v68, s[34:35]
	global_load_dwordx4 v[86:89], v69, s[34:35]
	global_load_dwordx4 v[90:93], v70, s[34:35]
	global_load_dwordx4 v[94:97], v71, s[34:35]
	global_load_dwordx4 v[98:101], v72, s[34:35]
	global_load_dwordx4 v[102:105], v73, s[34:35]
	v_and_b32_e32 v150, 15, v0
	v_or_b32_e32 v150, s24, v150
	v_and_b32_e32 v151, 48, v0
	v_lshl_or_b32 v150, v150, 10, v151
	global_load_dwordx4 v[62:65], v150, s[22:23] offset:0
	global_load_dwordx4 v[58:61], v150, s[22:23] offset:64
	global_load_dwordx4 v[54:57], v150, s[22:23] offset:128
	global_load_dwordx4 v[50:53], v150, s[22:23] offset:192
	global_load_dwordx4 v[46:49], v150, s[22:23] offset:256
	global_load_dwordx4 v[42:45], v150, s[22:23] offset:320
	global_load_dwordx4 v[38:41], v150, s[22:23] offset:384
	global_load_dwordx4 v[34:37], v150, s[22:23] offset:448
	global_load_dwordx4 v[30:33], v150, s[22:23] offset:512
	global_load_dwordx4 v[26:29], v150, s[22:23] offset:576
	global_load_dwordx4 v[22:25], v150, s[22:23] offset:640
	global_load_dwordx4 v[18:21], v150, s[22:23] offset:704
	global_load_dwordx4 v[14:17], v150, s[22:23] offset:768
	global_load_dwordx4 v[10:13], v150, s[22:23] offset:832
	global_load_dwordx4 v[6:9], v150, s[22:23] offset:896
	global_load_dwordx4 v[2:5], v150, s[22:23] offset:960
	v_mov_b32_e32 v142, 1
	v_mov_b32_e32 v143, 4
	v_mov_b32_e32 v144, 0x11100
	v_lshlrev_b32_e32 v145, 8, v0
	v_lshlrev_b32_e32 v148, 3, v0
	v_mov_b32_e32 v152, 0
	v_mov_b32_e32 v153, 0
	ds_write_b64 v148, v[152:153] offset:32768
	ds_write_b64 v148, v[152:153] offset:34832
	ds_write_b64 v148, v[152:153] offset:36896
	ds_write_b64 v148, v[152:153] offset:38960
	ds_write_b64 v148, v[152:153] offset:41024
	ds_write_b64 v148, v[152:153] offset:43088
	ds_write_b64 v148, v[152:153] offset:45152
	ds_write_b64 v148, v[152:153] offset:47216
	ds_write_b64 v148, v[152:153] offset:49280
	ds_write_b64 v148, v[152:153] offset:51344
	ds_write_b64 v148, v[152:153] offset:53408
	ds_write_b64 v148, v[152:153] offset:55472
	ds_write_b64 v148, v[152:153] offset:57536
	ds_write_b64 v148, v[152:153] offset:59600
	ds_write_b64 v148, v[152:153] offset:61664
	ds_write_b64 v148, v[152:153] offset:63728
	v_cmp_gt_u32_e32 vcc, 16, v0
	s_and_saveexec_b64 s[30:31], vcc
	v_lshl_add_u32 v151, v0, 2, v144
	ds_write_b32 v151, v152
	s_mov_b64 exec, s[30:31]
	s_waitcnt lgkmcnt(0)
	s_barrier
	s_waitcnt vmcnt(16)
	v_subrev_u32_e32 v74, s29, v74
	v_subrev_u32_e32 v75, s29, v75
	v_subrev_u32_e32 v76, s29, v76
	v_subrev_u32_e32 v77, s29, v77
	v_subrev_u32_e32 v78, s29, v78
	v_subrev_u32_e32 v79, s29, v79
	v_subrev_u32_e32 v80, s29, v80
	v_subrev_u32_e32 v81, s29, v81
	v_subrev_u32_e32 v82, s29, v82
	v_subrev_u32_e32 v83, s29, v83
	v_subrev_u32_e32 v84, s29, v84
	v_subrev_u32_e32 v85, s29, v85
	v_subrev_u32_e32 v86, s29, v86
	v_subrev_u32_e32 v87, s29, v87
	v_subrev_u32_e32 v88, s29, v88
	v_subrev_u32_e32 v89, s29, v89
	v_subrev_u32_e32 v90, s29, v90
	v_subrev_u32_e32 v91, s29, v91
	v_subrev_u32_e32 v92, s29, v92
	v_subrev_u32_e32 v93, s29, v93
	v_subrev_u32_e32 v94, s29, v94
	v_subrev_u32_e32 v95, s29, v95
	v_subrev_u32_e32 v96, s29, v96
	v_subrev_u32_e32 v97, s29, v97
	v_subrev_u32_e32 v98, s29, v98
	v_subrev_u32_e32 v99, s29, v99
	v_subrev_u32_e32 v100, s29, v100
	v_subrev_u32_e32 v101, s29, v101
	v_subrev_u32_e32 v102, s29, v102
	v_subrev_u32_e32 v103, s29, v103
	v_subrev_u32_e32 v104, s29, v104
	v_subrev_u32_e32 v105, s29, v105
	v_cmp_gt_u32_e64 s[36:37], 16, v74
	v_cmp_gt_u32_e64 s[38:39], 16, v75
	v_cmp_gt_u32_e64 s[40:41], 16, v76
	v_cmp_gt_u32_e64 s[42:43], 16, v77
	v_cmp_gt_u32_e64 s[44:45], 16, v78
	v_cmp_gt_u32_e64 s[46:47], 16, v79
	v_cmp_gt_u32_e64 s[48:49], 16, v80
	v_cmp_gt_u32_e64 s[50:51], 16, v81
	v_cmp_gt_u32_e64 s[52:53], 16, v82
	v_cmp_gt_u32_e64 s[54:55], 16, v83
	v_cmp_gt_u32_e64 s[56:57], 16, v84
	v_cmp_gt_u32_e64 s[58:59], 16, v85
	v_cmp_gt_u32_e64 s[60:61], 16, v86
	v_cmp_gt_u32_e64 s[62:63], 16, v87
	v_cmp_gt_u32_e64 s[64:65], 16, v88
	v_cmp_gt_u32_e64 s[66:67], 16, v89
	v_cmp_gt_u32_e64 s[68:69], 16, v90
	v_cmp_gt_u32_e64 s[70:71], 16, v91
	v_cmp_gt_u32_e64 s[72:73], 16, v92
	v_cmp_gt_u32_e64 s[74:75], 16, v93
	v_cmp_gt_u32_e64 s[76:77], 16, v94
	v_cmp_gt_u32_e64 s[78:79], 16, v95
	v_cmp_gt_u32_e64 s[80:81], 16, v96
	v_cmp_gt_u32_e64 s[82:83], 16, v97
	v_cmp_gt_u32_e64 s[84:85], 16, v98
	v_cmp_gt_u32_e64 s[86:87], 16, v99
	v_cmp_gt_u32_e64 s[88:89], 16, v100
	v_cmp_gt_u32_e64 s[90:91], 16, v101
	v_cmp_gt_u32_e64 s[92:93], 16, v102
	v_cmp_gt_u32_e64 s[94:95], 16, v103
	v_cmp_gt_u32_e64 s[96:97], 16, v104
	v_cmp_gt_u32_e64 s[98:99], 16, v105
	s_mov_b64 exec, s[36:37]
	v_lshl_add_u32 v74, v74, 2, v144
	ds_add_u32 v74, v142
	s_mov_b64 exec, s[38:39]
	v_lshl_add_u32 v75, v75, 2, v144
	ds_add_u32 v75, v142
	s_mov_b64 exec, s[40:41]
	v_lshl_add_u32 v76, v76, 2, v144
	ds_add_u32 v76, v142
	s_mov_b64 exec, s[42:43]
	v_lshl_add_u32 v77, v77, 2, v144
	ds_add_u32 v77, v142
	s_mov_b64 exec, s[44:45]
	v_lshl_add_u32 v78, v78, 2, v144
	ds_add_u32 v78, v142
	s_mov_b64 exec, s[46:47]
	v_lshl_add_u32 v79, v79, 2, v144
	ds_add_u32 v79, v142
	s_mov_b64 exec, s[48:49]
	v_lshl_add_u32 v80, v80, 2, v144
	ds_add_u32 v80, v142
	s_mov_b64 exec, s[50:51]
	v_lshl_add_u32 v81, v81, 2, v144
	ds_add_u32 v81, v142
	s_mov_b64 exec, s[52:53]
	v_lshl_add_u32 v82, v82, 2, v144
	ds_add_u32 v82, v142
	s_mov_b64 exec, s[54:55]
	v_lshl_add_u32 v83, v83, 2, v144
	ds_add_u32 v83, v142
	s_mov_b64 exec, s[56:57]
	v_lshl_add_u32 v84, v84, 2, v144
	ds_add_u32 v84, v142
	s_mov_b64 exec, s[58:59]
	v_lshl_add_u32 v85, v85, 2, v144
	ds_add_u32 v85, v142
	s_mov_b64 exec, s[60:61]
	v_lshl_add_u32 v86, v86, 2, v144
	ds_add_u32 v86, v142
	s_mov_b64 exec, s[62:63]
	v_lshl_add_u32 v87, v87, 2, v144
	ds_add_u32 v87, v142
	s_mov_b64 exec, s[64:65]
	v_lshl_add_u32 v88, v88, 2, v144
	ds_add_u32 v88, v142
	s_mov_b64 exec, s[66:67]
	v_lshl_add_u32 v89, v89, 2, v144
	ds_add_u32 v89, v142
	s_mov_b64 exec, s[68:69]
	v_lshl_add_u32 v90, v90, 2, v144
	ds_add_u32 v90, v142
	s_mov_b64 exec, s[70:71]
	v_lshl_add_u32 v91, v91, 2, v144
	ds_add_u32 v91, v142
	s_mov_b64 exec, s[72:73]
	v_lshl_add_u32 v92, v92, 2, v144
	ds_add_u32 v92, v142
	s_mov_b64 exec, s[74:75]
	v_lshl_add_u32 v93, v93, 2, v144
	ds_add_u32 v93, v142
	s_mov_b64 exec, s[76:77]
	v_lshl_add_u32 v94, v94, 2, v144
	ds_add_u32 v94, v142
	s_mov_b64 exec, s[78:79]
	v_lshl_add_u32 v95, v95, 2, v144
	ds_add_u32 v95, v142
	s_mov_b64 exec, s[80:81]
	v_lshl_add_u32 v96, v96, 2, v144
	ds_add_u32 v96, v142
	s_mov_b64 exec, s[82:83]
	v_lshl_add_u32 v97, v97, 2, v144
	ds_add_u32 v97, v142
	s_mov_b64 exec, s[84:85]
	v_lshl_add_u32 v98, v98, 2, v144
	ds_add_u32 v98, v142
	s_mov_b64 exec, s[86:87]
	v_lshl_add_u32 v99, v99, 2, v144
	ds_add_u32 v99, v142
	s_mov_b64 exec, s[88:89]
	v_lshl_add_u32 v100, v100, 2, v144
	ds_add_u32 v100, v142
	s_mov_b64 exec, s[90:91]
	v_lshl_add_u32 v101, v101, 2, v144
	ds_add_u32 v101, v142
	s_mov_b64 exec, s[92:93]
	v_lshl_add_u32 v102, v102, 2, v144
	ds_add_u32 v102, v142
	s_mov_b64 exec, s[94:95]
	v_lshl_add_u32 v103, v103, 2, v144
	ds_add_u32 v103, v142
	s_mov_b64 exec, s[96:97]
	v_lshl_add_u32 v104, v104, 2, v144
	ds_add_u32 v104, v142
	s_mov_b64 exec, s[98:99]
	v_lshl_add_u32 v105, v105, 2, v144
	ds_add_u32 v105, v142
	s_mov_b64 exec, -1
	s_waitcnt lgkmcnt(0)
	s_barrier
	v_and_b32_e32 v67, 15, v0
	v_lshl_add_u32 v67, v67, 2, v144
	ds_read_b32 v68, v67
	s_waitcnt vmcnt(0)
	v_fma_f32 v150, v62, v62, 0
	v_fmac_f32_e32 v150, v63, v63
	v_fmac_f32_e32 v150, v64, v64
	v_fmac_f32_e32 v150, v65, v65
	v_fmac_f32_e32 v150, v58, v58
	v_fmac_f32_e32 v150, v59, v59
	v_fmac_f32_e32 v150, v60, v60
	v_fmac_f32_e32 v150, v61, v61
	v_fmac_f32_e32 v150, v54, v54
	v_fmac_f32_e32 v150, v55, v55
	v_fmac_f32_e32 v150, v56, v56
	v_fmac_f32_e32 v150, v57, v57
	v_fmac_f32_e32 v150, v50, v50
	v_fmac_f32_e32 v150, v51, v51
	v_fmac_f32_e32 v150, v52, v52
	v_fmac_f32_e32 v150, v53, v53
	v_fmac_f32_e32 v150, v46, v46
	v_fmac_f32_e32 v150, v47, v47
	v_fmac_f32_e32 v150, v48, v48
	v_fmac_f32_e32 v150, v49, v49
	v_fmac_f32_e32 v150, v42, v42
	v_fmac_f32_e32 v150, v43, v43
	v_fmac_f32_e32 v150, v44, v44
	v_fmac_f32_e32 v150, v45, v45
	v_fmac_f32_e32 v150, v38, v38
	v_fmac_f32_e32 v150, v39, v39
	v_fmac_f32_e32 v150, v40, v40
	v_fmac_f32_e32 v150, v41, v41
	v_fmac_f32_e32 v150, v34, v34
	v_fmac_f32_e32 v150, v35, v35
	v_fmac_f32_e32 v150, v36, v36
	v_fmac_f32_e32 v150, v37, v37
	v_fmac_f32_e32 v150, v30, v30
	v_fmac_f32_e32 v150, v31, v31
	v_fmac_f32_e32 v150, v32, v32
	v_fmac_f32_e32 v150, v33, v33
	v_fmac_f32_e32 v150, v26, v26
	v_fmac_f32_e32 v150, v27, v27
	v_fmac_f32_e32 v150, v28, v28
	v_fmac_f32_e32 v150, v29, v29
	v_fmac_f32_e32 v150, v22, v22
	v_fmac_f32_e32 v150, v23, v23
	v_fmac_f32_e32 v150, v24, v24
	v_fmac_f32_e32 v150, v25, v25
	v_fmac_f32_e32 v150, v18, v18
	v_fmac_f32_e32 v150, v19, v19
	v_fmac_f32_e32 v150, v20, v20
	v_fmac_f32_e32 v150, v21, v21
	v_fmac_f32_e32 v150, v14, v14
	v_fmac_f32_e32 v150, v15, v15
	v_fmac_f32_e32 v150, v16, v16
	v_fmac_f32_e32 v150, v17, v17
	v_fmac_f32_e32 v150, v10, v10
	v_fmac_f32_e32 v150, v11, v11
	v_fmac_f32_e32 v150, v12, v12
	v_fmac_f32_e32 v150, v13, v13
	v_fmac_f32_e32 v150, v6, v6
	v_fmac_f32_e32 v150, v7, v7
	v_fmac_f32_e32 v150, v8, v8
	v_fmac_f32_e32 v150, v9, v9
	v_fmac_f32_e32 v150, v2, v2
	v_fmac_f32_e32 v150, v3, v3
	v_fmac_f32_e32 v150, v4, v4
	v_fmac_f32_e32 v150, v5, v5
	v_mbcnt_lo_u32_b32 v151, -1, 0
	v_mbcnt_hi_u32_b32 v151, -1, v151
	v_and_b32_e32 v153, 64, v151
	v_xor_b32_e32 v152, 16, v151
	v_add_u32_e32 v153, 64, v153
	v_cmp_lt_i32_e32 vcc, v152, v153
	s_nop 1
	v_cndmask_b32_e32 v152, v151, v152, vcc
	v_lshlrev_b32_e32 v152, 2, v152
	ds_bpermute_b32 v152, v152, v150
	s_waitcnt lgkmcnt(0)
	v_add_f32_e32 v150, v150, v152
	v_xor_b32_e32 v152, 32, v151
	v_cmp_lt_i32_e32 vcc, v152, v153
	s_nop 1
	v_cndmask_b32_e32 v151, v151, v152, vcc
	v_lshlrev_b32_e32 v151, 2, v151
	ds_bpermute_b32 v151, v151, v150
	v_mov_b32_e32 v69, v68
	s_nop 1
	v_add_u32_dpp v69, v69, v69 row_shr:1 row_mask:0xf bank_mask:0xf bound_ctrl:1
	s_nop 1
	v_add_u32_dpp v69, v69, v69 row_shr:2 row_mask:0xf bank_mask:0xf bound_ctrl:1
	s_nop 1
	v_add_u32_dpp v69, v69, v69 row_shr:4 row_mask:0xf bank_mask:0xf bound_ctrl:1
	s_nop 1
	v_add_u32_dpp v69, v69, v69 row_shr:8 row_mask:0xf bank_mask:0xf bound_ctrl:1
	s_nop 1
	v_sub_u32_e32 v70, v69, v68
	v_lshlrev_b32_e32 v70, 2, v70
	v_readlane_b32 s8, v69, 15
	v_cmp_gt_u32_e32 vcc, 16, v1
	s_and_saveexec_b64 s[30:31], vcc
	v_add_u32_e32 v152, s24, v1
	v_lshlrev_b32_e32 v152, 2, v152
	v_add_u32_e32 v152, 0x11300, v152
	s_waitcnt lgkmcnt(0)
	v_add_f32_e32 v150, v150, v151
	ds_write_b32 v152, v150
	s_cmp_lg_u32 s17, 0
	s_cbranch_scc1 .Lfront_nocursor
	ds_write_b32 v67, v70 offset:64
.Lfront_nocursor:
	s_mov_b64 exec, s[30:31]
	s_waitcnt lgkmcnt(0)
	s_barrier
	s_mov_b64 exec, s[36:37]
	ds_add_rtn_u32 v106, v74, v143 offset:64
	s_mov_b64 exec, s[38:39]
	ds_add_rtn_u32 v107, v75, v143 offset:64
	s_mov_b64 exec, s[40:41]
	ds_add_rtn_u32 v108, v76, v143 offset:64
	s_mov_b64 exec, s[42:43]
	ds_add_rtn_u32 v109, v77, v143 offset:64
	s_mov_b64 exec, s[44:45]
	ds_add_rtn_u32 v110, v78, v143 offset:64
	s_mov_b64 exec, s[46:47]
	ds_add_rtn_u32 v111, v79, v143 offset:64
	s_mov_b64 exec, s[48:49]
	ds_add_rtn_u32 v112, v80, v143 offset:64
	s_mov_b64 exec, s[50:51]
	ds_add_rtn_u32 v113, v81, v143 offset:64
	s_mov_b64 exec, s[52:53]
	ds_add_rtn_u32 v114, v82, v143 offset:64
	s_mov_b64 exec, s[54:55]
	ds_add_rtn_u32 v115, v83, v143 offset:64
	s_mov_b64 exec, s[56:57]
	ds_add_rtn_u32 v116, v84, v143 offset:64
	s_mov_b64 exec, s[58:59]
	ds_add_rtn_u32 v117, v85, v143 offset:64
	s_mov_b64 exec, s[60:61]
	ds_add_rtn_u32 v118, v86, v143 offset:64
	s_mov_b64 exec, s[62:63]
	ds_add_rtn_u32 v119, v87, v143 offset:64
	s_mov_b64 exec, s[64:65]
	ds_add_rtn_u32 v120, v88, v143 offset:64
	s_mov_b64 exec, s[66:67]
	ds_add_rtn_u32 v121, v89, v143 offset:64
	s_mov_b64 exec, s[68:69]
	ds_add_rtn_u32 v122, v90, v143 offset:64
	s_mov_b64 exec, s[70:71]
	ds_add_rtn_u32 v123, v91, v143 offset:64
	s_mov_b64 exec, s[72:73]
	ds_add_rtn_u32 v124, v92, v143 offset:64
	s_mov_b64 exec, s[74:75]
	ds_add_rtn_u32 v125, v93, v143 offset:64
	s_mov_b64 exec, s[76:77]
	ds_add_rtn_u32 v126, v94, v143 offset:64
	s_mov_b64 exec, s[78:79]
	ds_add_rtn_u32 v127, v95, v143 offset:64
	s_mov_b64 exec, s[80:81]
	ds_add_rtn_u32 v128, v96, v143 offset:64
	s_mov_b64 exec, s[82:83]
	ds_add_rtn_u32 v129, v97, v143 offset:64
	s_mov_b64 exec, s[84:85]
	ds_add_rtn_u32 v130, v98, v143 offset:64
	s_mov_b64 exec, s[86:87]
	ds_add_rtn_u32 v131, v99, v143 offset:64
	s_mov_b64 exec, s[88:89]
	ds_add_rtn_u32 v132, v100, v143 offset:64
	s_mov_b64 exec, s[90:91]
	ds_add_rtn_u32 v133, v101, v143 offset:64
	s_mov_b64 exec, s[92:93]
	ds_add_rtn_u32 v134, v102, v143 offset:64
	s_mov_b64 exec, s[94:95]
	ds_add_rtn_u32 v135, v103, v143 offset:64
	s_mov_b64 exec, s[96:97]
	ds_add_rtn_u32 v136, v104, v143 offset:64
	s_mov_b64 exec, s[98:99]
	ds_add_rtn_u32 v137, v105, v143 offset:64
	s_mov_b64 exec, -1
	v_add_u32_e32 v146, 0x0, v145
	v_and_or_b32 v146, v74, 60, v146
	s_waitcnt lgkmcnt(0)
	s_mov_b64 exec, s[36:37]
	ds_write_b32 v106, v146
	s_mov_b64 exec, -1
	v_add_u32_e32 v147, 0x40, v145
	v_and_or_b32 v147, v75, 60, v147
	s_mov_b64 exec, s[38:39]
	ds_write_b32 v107, v147
	s_mov_b64 exec, -1
	v_add_u32_e32 v146, 0x80, v145
	v_and_or_b32 v146, v76, 60, v146
	s_mov_b64 exec, s[40:41]
	ds_write_b32 v108, v146
	s_mov_b64 exec, -1
	v_add_u32_e32 v147, 0xc0, v145
	v_and_or_b32 v147, v77, 60, v147
	s_mov_b64 exec, s[42:43]
	ds_write_b32 v109, v147
	s_mov_b64 exec, -1
	v_add_u32_e32 v146, 0x10000, v145
	v_and_or_b32 v146, v78, 60, v146
	s_mov_b64 exec, s[44:45]
	ds_write_b32 v110, v146
	s_mov_b64 exec, -1
	v_add_u32_e32 v147, 0x10040, v145
	v_and_or_b32 v147, v79, 60, v147
	s_mov_b64 exec, s[46:47]
	ds_write_b32 v111, v147
	s_mov_b64 exec, -1
	v_add_u32_e32 v146, 0x10080, v145
	v_and_or_b32 v146, v80, 60, v146
	s_mov_b64 exec, s[48:49]
	ds_write_b32 v112, v146
	s_mov_b64 exec, -1
	v_add_u32_e32 v147, 0x100c0, v145
	v_and_or_b32 v147, v81, 60, v147
	s_mov_b64 exec, s[50:51]
	ds_write_b32 v113, v147
	s_mov_b64 exec, -1
	v_add_u32_e32 v146, 0x20000, v145
	v_and_or_b32 v146, v82, 60, v146
	s_mov_b64 exec, s[52:53]
	ds_write_b32 v114, v146
	s_mov_b64 exec, -1
	v_add_u32_e32 v147, 0x20040, v145
	v_and_or_b32 v147, v83, 60, v147
	s_mov_b64 exec, s[54:55]
	ds_write_b32 v115, v147
	s_mov_b64 exec, -1
	v_add_u32_e32 v146, 0x20080, v145
	v_and_or_b32 v146, v84, 60, v146
	s_mov_b64 exec, s[56:57]
	ds_write_b32 v116, v146
	s_mov_b64 exec, -1
	v_add_u32_e32 v147, 0x200c0, v145
	v_and_or_b32 v147, v85, 60, v147
	s_mov_b64 exec, s[58:59]
	ds_write_b32 v117, v147
	s_mov_b64 exec, -1
	v_add_u32_e32 v146, 0x30000, v145
	v_and_or_b32 v146, v86, 60, v146
	s_mov_b64 exec, s[60:61]
	ds_write_b32 v118, v146
	s_mov_b64 exec, -1
	v_add_u32_e32 v147, 0x30040, v145
	v_and_or_b32 v147, v87, 60, v147
	s_mov_b64 exec, s[62:63]
	ds_write_b32 v119, v147
	s_mov_b64 exec, -1
	v_add_u32_e32 v146, 0x30080, v145
	v_and_or_b32 v146, v88, 60, v146
	s_mov_b64 exec, s[64:65]
	ds_write_b32 v120, v146
	s_mov_b64 exec, -1
	v_add_u32_e32 v147, 0x300c0, v145
	v_and_or_b32 v147, v89, 60, v147
	s_mov_b64 exec, s[66:67]
	ds_write_b32 v121, v147
	s_mov_b64 exec, -1
	v_add_u32_e32 v146, 0x40000, v145
	v_and_or_b32 v146, v90, 60, v146
	s_mov_b64 exec, s[68:69]
	ds_write_b32 v122, v146
	s_mov_b64 exec, -1
	v_add_u32_e32 v147, 0x40040, v145
	v_and_or_b32 v147, v91, 60, v147
	s_mov_b64 exec, s[70:71]
	ds_write_b32 v123, v147
	s_mov_b64 exec, -1
	v_add_u32_e32 v146, 0x40080, v145
	v_and_or_b32 v146, v92, 60, v146
	s_mov_b64 exec, s[72:73]
	ds_write_b32 v124, v146
	s_mov_b64 exec, -1
	v_add_u32_e32 v147, 0x400c0, v145
	v_and_or_b32 v147, v93, 60, v147
	s_mov_b64 exec, s[74:75]
	ds_write_b32 v125, v147
	s_mov_b64 exec, -1
	v_add_u32_e32 v146, 0x50000, v145
	v_and_or_b32 v146, v94, 60, v146
	s_mov_b64 exec, s[76:77]
	ds_write_b32 v126, v146
	s_mov_b64 exec, -1
	v_add_u32_e32 v147, 0x50040, v145
	v_and_or_b32 v147, v95, 60, v147
	s_mov_b64 exec, s[78:79]
	ds_write_b32 v127, v147
	s_mov_b64 exec, -1
	v_add_u32_e32 v146, 0x50080, v145
	v_and_or_b32 v146, v96, 60, v146
	s_mov_b64 exec, s[80:81]
	ds_write_b32 v128, v146
	s_mov_b64 exec, -1
	v_add_u32_e32 v147, 0x500c0, v145
	v_and_or_b32 v147, v97, 60, v147
	s_mov_b64 exec, s[82:83]
	ds_write_b32 v129, v147
	s_mov_b64 exec, -1
	v_add_u32_e32 v146, 0x60000, v145
	v_and_or_b32 v146, v98, 60, v146
	s_mov_b64 exec, s[84:85]
	ds_write_b32 v130, v146
	s_mov_b64 exec, -1
	v_add_u32_e32 v147, 0x60040, v145
	v_and_or_b32 v147, v99, 60, v147
	s_mov_b64 exec, s[86:87]
	ds_write_b32 v131, v147
	s_mov_b64 exec, -1
	v_add_u32_e32 v146, 0x60080, v145
	v_and_or_b32 v146, v100, 60, v146
	s_mov_b64 exec, s[88:89]
	ds_write_b32 v132, v146
	s_mov_b64 exec, -1
	v_add_u32_e32 v147, 0x600c0, v145
	v_and_or_b32 v147, v101, 60, v147
	s_mov_b64 exec, s[90:91]
	ds_write_b32 v133, v147
	s_mov_b64 exec, -1
	v_add_u32_e32 v146, 0x70000, v145
	v_and_or_b32 v146, v102, 60, v146
	s_mov_b64 exec, s[92:93]
	ds_write_b32 v134, v146
	s_mov_b64 exec, -1
	v_add_u32_e32 v147, 0x70040, v145
	v_and_or_b32 v147, v103, 60, v147
	s_mov_b64 exec, s[94:95]
	ds_write_b32 v135, v147
	s_mov_b64 exec, -1
	v_add_u32_e32 v146, 0x70080, v145
	v_and_or_b32 v146, v104, 60, v146
	s_mov_b64 exec, s[96:97]
	ds_write_b32 v136, v146
	s_mov_b64 exec, -1
	v_add_u32_e32 v147, 0x700c0, v145
	v_and_or_b32 v147, v105, 60, v147
	s_mov_b64 exec, s[98:99]
	ds_write_b32 v137, v147
	s_mov_b64 exec, -1
	s_waitcnt lgkmcnt(0)
	s_barrier
	s_mul_i32 s37, s8, s17
	s_lshr_b32 s37, s37, 2
	s_add_i32 s38, s17, 1
	s_mul_i32 s38, s8, s38
	s_lshr_b32 s38, s38, 2
	v_lshlrev_b32_e32 v218, 4, v1
	v_lshlrev_b32_e32 v219, 3, v1
	v_mov_b32_e32 v200, 0
	v_mov_b32_e32 v201, 0
	v_mov_b32_e32 v202, 0
	v_mov_b32_e32 v203, 0
	v_mov_b32_e32 v204, 0
	v_mov_b32_e32 v205, 0
	v_mov_b32_e32 v206, 0
	v_mov_b32_e32 v207, 0
	s_cmp_ge_u32 s37, s38
	s_cbranch_scc1 .Lg_alldone
	s_mov_b32 s50, -1
.Lg_block:
	s_sub_u32 s39, s38, s37
	s_min_u32 s39, s39, 0x80
	v_add_u32_e32 v221, s37, v1
	v_lshlrev_b32_e32 v221, 2, v221
	ds_read_b32 v216, v221
	ds_read_b32 v217, v221 offset:256
	s_waitcnt lgkmcnt(0)
	s_cmp_lg_u32 s50, -1
	s_cbranch_scc1 .Lg_havecur
	v_readlane_b32 s50, v216, 0
	s_bfe_u32 s50, s50, 0x40002
.Lg_havecur:
	s_cmp_gt_u32 s39, 0
	s_cbranch_scc0 .Lg_prodone
	s_mov_b32 s41, 0
	s_and_b32 s46, s41, 63
	v_readlane_b32 s40, v216, s46
	v_readlane_b32 s47, v217, s46
	s_cmp_lt_u32 s41, 64
	s_cselect_b32 s40, s40, s47
	s_bfe_u32 s60, s40, 0x40002
	s_and_b32 s40, s40, 0xffffffc0
	s_lshl_b32 s40, s40, 4
	s_add_u32 s42, s32, s40
	s_addc_u32 s43, s33, 0
	global_load_dwordx4 v[66:69], v218, s[42:43] nt
	s_cmp_gt_u32 s39, 1
	s_cbranch_scc0 .Lg_prodone
	s_mov_b32 s41, 1
	s_and_b32 s46, s41, 63
	v_readlane_b32 s40, v216, s46
	v_readlane_b32 s47, v217, s46
	s_cmp_lt_u32 s41, 64
	s_cselect_b32 s40, s40, s47
	s_bfe_u32 s61, s40, 0x40002
	s_and_b32 s40, s40, 0xffffffc0
	s_lshl_b32 s40, s40, 4
	s_add_u32 s42, s32, s40
	s_addc_u32 s43, s33, 0
	global_load_dwordx4 v[70:73], v218, s[42:43] nt
	s_cmp_gt_u32 s39, 2
	s_cbranch_scc0 .Lg_prodone
	s_mov_b32 s41, 2
	s_and_b32 s46, s41, 63
	v_readlane_b32 s40, v216, s46
	v_readlane_b32 s47, v217, s46
	s_cmp_lt_u32 s41, 64
	s_cselect_b32 s40, s40, s47
	s_bfe_u32 s62, s40, 0x40002
	s_and_b32 s40, s40, 0xffffffc0
	s_lshl_b32 s40, s40, 4
	s_add_u32 s42, s32, s40
	s_addc_u32 s43, s33, 0
	global_load_dwordx4 v[74:77], v218, s[42:43] nt
	s_cmp_gt_u32 s39, 3
	s_cbranch_scc0 .Lg_prodone
	s_mov_b32 s41, 3
	s_and_b32 s46, s41, 63
	v_readlane_b32 s40, v216, s46
	v_readlane_b32 s47, v217, s46
	s_cmp_lt_u32 s41, 64
	s_cselect_b32 s40, s40, s47
	s_bfe_u32 s63, s40, 0x40002
	s_and_b32 s40, s40, 0xffffffc0
	s_lshl_b32 s40, s40, 4
	s_add_u32 s42, s32, s40
	s_addc_u32 s43, s33, 0
	global_load_dwordx4 v[78:81], v218, s[42:43] nt
	s_cmp_gt_u32 s39, 4
	s_cbranch_scc0 .Lg_prodone
	s_mov_b32 s41, 4
	s_and_b32 s46, s41, 63
	v_readlane_b32 s40, v216, s46
	v_readlane_b32 s47, v217, s46
	s_cmp_lt_u32 s41, 64
	s_cselect_b32 s40, s40, s47
	s_bfe_u32 s64, s40, 0x40002
	s_and_b32 s40, s40, 0xffffffc0
	s_lshl_b32 s40, s40, 4
	s_add_u32 s42, s32, s40
	s_addc_u32 s43, s33, 0
	global_load_dwordx4 v[82:85], v218, s[42:43] nt
	s_cmp_gt_u32 s39, 5
	s_cbranch_scc0 .Lg_prodone
	s_mov_b32 s41, 5
	s_and_b32 s46, s41, 63
	v_readlane_b32 s40, v216, s46
	v_readlane_b32 s47, v217, s46
	s_cmp_lt_u32 s41, 64
	s_cselect_b32 s40, s40, s47
	s_bfe_u32 s65, s40, 0x40002
	s_and_b32 s40, s40, 0xffffffc0
	s_lshl_b32 s40, s40, 4
	s_add_u32 s42, s32, s40
	s_addc_u32 s43, s33, 0
	global_load_dwordx4 v[86:89], v218, s[42:43] nt
	s_cmp_gt_u32 s39, 6
	s_cbranch_scc0 .Lg_prodone
	s_mov_b32 s41, 6
	s_and_b32 s46, s41, 63
	v_readlane_b32 s40, v216, s46
	v_readlane_b32 s47, v217, s46
	s_cmp_lt_u32 s41, 64
	s_cselect_b32 s40, s40, s47
	s_bfe_u32 s66, s40, 0x40002
	s_and_b32 s40, s40, 0xffffffc0
	s_lshl_b32 s40, s40, 4
	s_add_u32 s42, s32, s40
	s_addc_u32 s43, s33, 0
	global_load_dwordx4 v[90:93], v218, s[42:43] nt
	s_cmp_gt_u32 s39, 7
	s_cbranch_scc0 .Lg_prodone
	s_mov_b32 s41, 7
	s_and_b32 s46, s41, 63
	v_readlane_b32 s40, v216, s46
	v_readlane_b32 s47, v217, s46
	s_cmp_lt_u32 s41, 64
	s_cselect_b32 s40, s40, s47
	s_bfe_u32 s67, s40, 0x40002
	s_and_b32 s40, s40, 0xffffffc0
	s_lshl_b32 s40, s40, 4
	s_add_u32 s42, s32, s40
	s_addc_u32 s43, s33, 0
	global_load_dwordx4 v[94:97], v218, s[42:43] nt
	s_cmp_gt_u32 s39, 8
	s_cbranch_scc0 .Lg_prodone
	s_mov_b32 s41, 8
	s_and_b32 s46, s41, 63
	v_readlane_b32 s40, v216, s46
	v_readlane_b32 s47, v217, s46
	s_cmp_lt_u32 s41, 64
	s_cselect_b32 s40, s40, s47
	s_bfe_u32 s68, s40, 0x40002
	s_and_b32 s40, s40, 0xffffffc0
	s_lshl_b32 s40, s40, 4
	s_add_u32 s42, s32, s40
	s_addc_u32 s43, s33, 0
	global_load_dwordx4 v[98:101], v218, s[42:43] nt
	s_cmp_gt_u32 s39, 9
	s_cbranch_scc0 .Lg_prodone
	s_mov_b32 s41, 9
	s_and_b32 s46, s41, 63
	v_readlane_b32 s40, v216, s46
	v_readlane_b32 s47, v217, s46
	s_cmp_lt_u32 s41, 64
	s_cselect_b32 s40, s40, s47
	s_bfe_u32 s69, s40, 0x40002
	s_and_b32 s40, s40, 0xffffffc0
	s_lshl_b32 s40, s40, 4
	s_add_u32 s42, s32, s40
	s_addc_u32 s43, s33, 0
	global_load_dwordx4 v[102:105], v218, s[42:43] nt
	s_cmp_gt_u32 s39, 10
	s_cbranch_scc0 .Lg_prodone
	s_mov_b32 s41, 10
	s_and_b32 s46, s41, 63
	v_readlane_b32 s40, v216, s46
	v_readlane_b32 s47, v217, s46
	s_cmp_lt_u32 s41, 64
	s_cselect_b32 s40, s40, s47
	s_bfe_u32 s70, s40, 0x40002
	s_and_b32 s40, s40, 0xffffffc0
	s_lshl_b32 s40, s40, 4
	s_add_u32 s42, s32, s40
	s_addc_u32 s43, s33, 0
	global_load_dwordx4 v[106:109], v218, s[42:43] nt
	s_cmp_gt_u32 s39, 11
	s_cbranch_scc0 .Lg_prodone
	s_mov_b32 s41, 11
	s_and_b32 s46, s41, 63
	v_readlane_b32 s40, v216, s46
	v_readlane_b32 s47, v217, s46
	s_cmp_lt_u32 s41, 64
	s_cselect_b32 s40, s40, s47
	s_bfe_u32 s71, s40, 0x40002
	s_and_b32 s40, s40, 0xffffffc0
	s_lshl_b32 s40, s40, 4
	s_add_u32 s42, s32, s40
	s_addc_u32 s43, s33, 0
	global_load_dwordx4 v[110:113], v218, s[42:43] nt
	s_cmp_gt_u32 s39, 12
	s_cbranch_scc0 .Lg_prodone
	s_mov_b32 s41, 12
	s_and_b32 s46, s41, 63
	v_readlane_b32 s40, v216, s46
	v_readlane_b32 s47, v217, s46
	s_cmp_lt_u32 s41, 64
	s_cselect_b32 s40, s40, s47
	s_bfe_u32 s72, s40, 0x40002
	s_and_b32 s40, s40, 0xffffffc0
	s_lshl_b32 s40, s40, 4
	s_add_u32 s42, s32, s40
	s_addc_u32 s43, s33, 0
	global_load_dwordx4 v[114:117], v218, s[42:43] nt
	s_cmp_gt_u32 s39, 13
	s_cbranch_scc0 .Lg_prodone
	s_mov_b32 s41, 13
	s_and_b32 s46, s41, 63
	v_readlane_b32 s40, v216, s46
	v_readlane_b32 s47, v217, s46
	s_cmp_lt_u32 s41, 64
	s_cselect_b32 s40, s40, s47
	s_bfe_u32 s73, s40, 0x40002
	s_and_b32 s40, s40, 0xffffffc0
	s_lshl_b32 s40, s40, 4
	s_add_u32 s42, s32, s40
	s_addc_u32 s43, s33, 0
	global_load_dwordx4 v[118:121], v218, s[42:43] nt
	s_cmp_gt_u32 s39, 14
	s_cbranch_scc0 .Lg_prodone
	s_mov_b32 s41, 14
	s_and_b32 s46, s41, 63
	v_readlane_b32 s40, v216, s46
	v_readlane_b32 s47, v217, s46
	s_cmp_lt_u32 s41, 64
	s_cselect_b32 s40, s40, s47
	s_bfe_u32 s74, s40, 0x40002
	s_and_b32 s40, s40, 0xffffffc0
	s_lshl_b32 s40, s40, 4
	s_add_u32 s42, s32, s40
	s_addc_u32 s43, s33, 0
	global_load_dwordx4 v[122:125], v218, s[42:43] nt
	s_cmp_gt_u32 s39, 15
	s_cbranch_scc0 .Lg_prodone
	s_mov_b32 s41, 15
	s_and_b32 s46, s41, 63
	v_readlane_b32 s40, v216, s46
	v_readlane_b32 s47, v217, s46
	s_cmp_lt_u32 s41, 64
	s_cselect_b32 s40, s40, s47
	s_bfe_u32 s75, s40, 0x40002
	s_and_b32 s40, s40, 0xffffffc0
	s_lshl_b32 s40, s40, 4
	s_add_u32 s42, s32, s40
	s_addc_u32 s43, s33, 0
	global_load_dwordx4 v[126:129], v218, s[42:43] nt
	s_cmp_gt_u32 s39, 16
	s_cbranch_scc0 .Lg_prodone
	s_mov_b32 s41, 16
	s_and_b32 s46, s41, 63
	v_readlane_b32 s40, v216, s46
	v_readlane_b32 s47, v217, s46
	s_cmp_lt_u32 s41, 64
	s_cselect_b32 s40, s40, s47
	s_bfe_u32 s76, s40, 0x40002
	s_and_b32 s40, s40, 0xffffffc0
	s_lshl_b32 s40, s40, 4
	s_add_u32 s42, s32, s40
	s_addc_u32 s43, s33, 0
	global_load_dwordx4 v[130:133], v218, s[42:43] nt
	s_cmp_gt_u32 s39, 17
	s_cbranch_scc0 .Lg_prodone
	s_mov_b32 s41, 17
	s_and_b32 s46, s41, 63
	v_readlane_b32 s40, v216, s46
	v_readlane_b32 s47, v217, s46
	s_cmp_lt_u32 s41, 64
	s_cselect_b32 s40, s40, s47
	s_bfe_u32 s77, s40, 0x40002
	s_and_b32 s40, s40, 0xffffffc0
	s_lshl_b32 s40, s40, 4
	s_add_u32 s42, s32, s40
	s_addc_u32 s43, s33, 0
	global_load_dwordx4 v[134:137], v218, s[42:43] nt
	s_cmp_gt_u32 s39, 18
	s_cbranch_scc0 .Lg_prodone
	s_mov_b32 s41, 18
	s_and_b32 s46, s41, 63
	v_readlane_b32 s40, v216, s46
	v_readlane_b32 s47, v217, s46
	s_cmp_lt_u32 s41, 64
	s_cselect_b32 s40, s40, s47
	s_bfe_u32 s78, s40, 0x40002
	s_and_b32 s40, s40, 0xffffffc0
	s_lshl_b32 s40, s40, 4
	s_add_u32 s42, s32, s40
	s_addc_u32 s43, s33, 0
	global_load_dwordx4 v[138:141], v218, s[42:43] nt
	s_cmp_gt_u32 s39, 19
	s_cbranch_scc0 .Lg_prodone
	s_mov_b32 s41, 19
	s_and_b32 s46, s41, 63
	v_readlane_b32 s40, v216, s46
	v_readlane_b32 s47, v217, s46
	s_cmp_lt_u32 s41, 64
	s_cselect_b32 s40, s40, s47
	s_bfe_u32 s79, s40, 0x40002
	s_and_b32 s40, s40, 0xffffffc0
	s_lshl_b32 s40, s40, 4
	s_add_u32 s42, s32, s40
	s_addc_u32 s43, s33, 0
	global_load_dwordx4 v[142:145], v218, s[42:43] nt
	s_cmp_gt_u32 s39, 20
	s_cbranch_scc0 .Lg_prodone
	s_mov_b32 s41, 20
	s_and_b32 s46, s41, 63
	v_readlane_b32 s40, v216, s46
	v_readlane_b32 s47, v217, s46
	s_cmp_lt_u32 s41, 64
	s_cselect_b32 s40, s40, s47
	s_bfe_u32 s80, s40, 0x40002
	s_and_b32 s40, s40, 0xffffffc0
	s_lshl_b32 s40, s40, 4
	s_add_u32 s42, s32, s40
	s_addc_u32 s43, s33, 0
	global_load_dwordx4 v[146:149], v218, s[42:43] nt
	s_cmp_gt_u32 s39, 21
	s_cbranch_scc0 .Lg_prodone
	s_mov_b32 s41, 21
	s_and_b32 s46, s41, 63
	v_readlane_b32 s40, v216, s46
	v_readlane_b32 s47, v217, s46
	s_cmp_lt_u32 s41, 64
	s_cselect_b32 s40, s40, s47
	s_bfe_u32 s81, s40, 0x40002
	s_and_b32 s40, s40, 0xffffffc0
	s_lshl_b32 s40, s40, 4
	s_add_u32 s42, s32, s40
	s_addc_u32 s43, s33, 0
	global_load_dwordx4 v[150:153], v218, s[42:43] nt
	s_cmp_gt_u32 s39, 22
	s_cbranch_scc0 .Lg_prodone
	s_mov_b32 s41, 22
	s_and_b32 s46, s41, 63
	v_readlane_b32 s40, v216, s46
	v_readlane_b32 s47, v217, s46
	s_cmp_lt_u32 s41, 64
	s_cselect_b32 s40, s40, s47
	s_bfe_u32 s82, s40, 0x40002
	s_and_b32 s40, s40, 0xffffffc0
	s_lshl_b32 s40, s40, 4
	s_add_u32 s42, s32, s40
	s_addc_u32 s43, s33, 0
	global_load_dwordx4 v[154:157], v218, s[42:43] nt
	s_cmp_gt_u32 s39, 23
	s_cbranch_scc0 .Lg_prodone
	s_mov_b32 s41, 23
	s_and_b32 s46, s41, 63
	v_readlane_b32 s40, v216, s46
	v_readlane_b32 s47, v217, s46
	s_cmp_lt_u32 s41, 64
	s_cselect_b32 s40, s40, s47
	s_bfe_u32 s83, s40, 0x40002
	s_and_b32 s40, s40, 0xffffffc0
	s_lshl_b32 s40, s40, 4
	s_add_u32 s42, s32, s40
	s_addc_u32 s43, s33, 0
	global_load_dwordx4 v[158:161], v218, s[42:43] nt
.Lg_prodone:
	s_mov_b32 s44, 0
	s_cmp_ge_u32 s39, 24
	s_cbranch_scc1 .Lg_slot0
	s_waitcnt vmcnt(0)
.Lg_slot0:
	s_waitcnt vmcnt(23)
	s_cmp_lg_u32 s60, s50
	s_cbranch_scc1 .Lg_flush0
.Lg_cont0:
	v_cvt_f64_f32_e32 v[208:209], v66
	v_cvt_f64_f32_e32 v[210:211], v67
	v_cvt_f64_f32_e32 v[212:213], v68
	v_cvt_f64_f32_e32 v[214:215], v69
	v_add_f64 v[200:201], v[200:201], v[208:209]
	v_add_f64 v[202:203], v[202:203], v[210:211]
	v_add_f64 v[204:205], v[204:205], v[212:213]
	v_add_f64 v[206:207], v[206:207], v[214:215]
	s_add_u32 s41, s44, 24
	s_cmp_lt_u32 s41, s39
	s_cbranch_scc0 .Lg_tail0
	s_and_b32 s46, s41, 63
	v_readlane_b32 s40, v216, s46
	v_readlane_b32 s47, v217, s46
	s_cmp_lt_u32 s41, 64
	s_cselect_b32 s40, s40, s47
	s_bfe_u32 s60, s40, 0x40002
	s_and_b32 s40, s40, 0xffffffc0
	s_lshl_b32 s40, s40, 4
	s_add_u32 s42, s32, s40
	s_addc_u32 s43, s33, 0
	global_load_dwordx4 v[66:69], v218, s[42:43] nt
.Lg_next0:
	s_add_u32 s44, s44, 1
	s_cmp_lt_u32 s44, s39
	s_cbranch_scc0 .Lg_blockdone
.Lg_slot1:
	s_waitcnt vmcnt(23)
	s_cmp_lg_u32 s61, s50
	s_cbranch_scc1 .Lg_flush1
.Lg_cont1:
	v_cvt_f64_f32_e32 v[208:209], v70
	v_cvt_f64_f32_e32 v[210:211], v71
	v_cvt_f64_f32_e32 v[212:213], v72
	v_cvt_f64_f32_e32 v[214:215], v73
	v_add_f64 v[200:201], v[200:201], v[208:209]
	v_add_f64 v[202:203], v[202:203], v[210:211]
	v_add_f64 v[204:205], v[204:205], v[212:213]
	v_add_f64 v[206:207], v[206:207], v[214:215]
	s_add_u32 s41, s44, 24
	s_cmp_lt_u32 s41, s39
	s_cbranch_scc0 .Lg_tail1
	s_and_b32 s46, s41, 63
	v_readlane_b32 s40, v216, s46
	v_readlane_b32 s47, v217, s46
	s_cmp_lt_u32 s41, 64
	s_cselect_b32 s40, s40, s47
	s_bfe_u32 s61, s40, 0x40002
	s_and_b32 s40, s40, 0xffffffc0
	s_lshl_b32 s40, s40, 4
	s_add_u32 s42, s32, s40
	s_addc_u32 s43, s33, 0
	global_load_dwordx4 v[70:73], v218, s[42:43] nt

.Lg_slot2:
	s_waitcnt vmcnt(23)
	s_cmp_lg_u32 s62, s50
	s_cbranch_scc1 .Lg_flush2
.Lg_cont2:
	v_cvt_f64_f32_e32 v[208:209], v74
	v_cvt_f64_f32_e32 v[210:211], v75
	v_cvt_f64_f32_e32 v[212:213], v76
	v_cvt_f64_f32_e32 v[214:215], v77
	v_add_f64 v[200:201], v[200:201], v[208:209]
	v_add_f64 v[202:203], v[202:203], v[210:211]
	v_add_f64 v[204:205], v[204:205], v[212:213]
	v_add_f64 v[206:207], v[206:207], v[214:215]
	s_add_u32 s41, s44, 24
	s_cmp_lt_u32 s41, s39
	s_cbranch_scc0 .Lg_tail2
	s_and_b32 s46, s41, 63
	v_readlane_b32 s40, v216, s46
	v_readlane_b32 s47, v217, s46
	s_cmp_lt_u32 s41, 64
	s_cselect_b32 s40, s40, s47
	s_bfe_u32 s62, s40, 0x40002
	s_and_b32 s40, s40, 0xffffffc0
	s_lshl_b32 s40, s40, 4
	s_add_u32 s42, s32, s40
	s_addc_u32 s43, s33, 0
	global_load_dwordx4 v[74:77], v218, s[42:43] nt

.Lg_slot3:
	s_waitcnt vmcnt(23)
	s_cmp_lg_u32 s63, s50
	s_cbranch_scc1 .Lg_flush3
.Lg_cont3:
	v_cvt_f64_f32_e32 v[208:209], v78
	v_cvt_f64_f32_e32 v[210:211], v79
	v_cvt_f64_f32_e32 v[212:213], v80
	v_cvt_f64_f32_e32 v[214:215], v81
	v_add_f64 v[200:201], v[200:201], v[208:209]
	v_add_f64 v[202:203], v[202:203], v[210:211]
	v_add_f64 v[204:205], v[204:205], v[212:213]
	v_add_f64 v[206:207], v[206:207], v[214:215]
	s_add_u32 s41, s44, 24
	s_cmp_lt_u32 s41, s39
	s_cbranch_scc0 .Lg_tail3
	s_and_b32 s46, s41, 63
	v_readlane_b32 s40, v216, s46
	v_readlane_b32 s47, v217, s46
	s_cmp_lt_u32 s41, 64
	s_cselect_b32 s40, s40, s47
	s_bfe_u32 s63, s40, 0x40002
	s_and_b32 s40, s40, 0xffffffc0
	s_lshl_b32 s40, s40, 4
	s_add_u32 s42, s32, s40
	s_addc_u32 s43, s33, 0
	global_load_dwordx4 v[78:81], v218, s[42:43] nt

.Lg_slot4:
	s_waitcnt vmcnt(23)
	s_cmp_lg_u32 s64, s50
	s_cbranch_scc1 .Lg_flush4
.Lg_cont4:
	v_cvt_f64_f32_e32 v[208:209], v82
	v_cvt_f64_f32_e32 v[210:211], v83
	v_cvt_f64_f32_e32 v[212:213], v84
	v_cvt_f64_f32_e32 v[214:215], v85
	v_add_f64 v[200:201], v[200:201], v[208:209]
	v_add_f64 v[202:203], v[202:203], v[210:211]
	v_add_f64 v[204:205], v[204:205], v[212:213]
	v_add_f64 v[206:207], v[206:207], v[214:215]
	s_add_u32 s41, s44, 24
	s_cmp_lt_u32 s41, s39
	s_cbranch_scc0 .Lg_tail4
	s_and_b32 s46, s41, 63
	v_readlane_b32 s40, v216, s46
	v_readlane_b32 s47, v217, s46
	s_cmp_lt_u32 s41, 64
	s_cselect_b32 s40, s40, s47
	s_bfe_u32 s64, s40, 0x40002
	s_and_b32 s40, s40, 0xffffffc0
	s_lshl_b32 s40, s40, 4
	s_add_u32 s42, s32, s40
	s_addc_u32 s43, s33, 0
	global_load_dwordx4 v[82:85], v218, s[42:43] nt

.Lg_slot5:
	s_waitcnt vmcnt(23)
	s_cmp_lg_u32 s65, s50
	s_cbranch_scc1 .Lg_flush5
.Lg_cont5:
	v_cvt_f64_f32_e32 v[208:209], v86
	v_cvt_f64_f32_e32 v[210:211], v87
	v_cvt_f64_f32_e32 v[212:213], v88
	v_cvt_f64_f32_e32 v[214:215], v89
	v_add_f64 v[200:201], v[200:201], v[208:209]
	v_add_f64 v[202:203], v[202:203], v[210:211]
	v_add_f64 v[204:205], v[204:205], v[212:213]
	v_add_f64 v[206:207], v[206:207], v[214:215]
	s_add_u32 s41, s44, 24
	s_cmp_lt_u32 s41, s39
	s_cbranch_scc0 .Lg_tail5
	s_and_b32 s46, s41, 63
	v_readlane_b32 s40, v216, s46
	v_readlane_b32 s47, v217, s46
	s_cmp_lt_u32 s41, 64
	s_cselect_b32 s40, s40, s47
	s_bfe_u32 s65, s40, 0x40002
	s_and_b32 s40, s40, 0xffffffc0
	s_lshl_b32 s40, s40, 4
	s_add_u32 s42, s32, s40
	s_addc_u32 s43, s33, 0
	global_load_dwordx4 v[86:89], v218, s[42:43] nt

.Lg_slot6:
	s_waitcnt vmcnt(23)
	s_cmp_lg_u32 s66, s50
	s_cbranch_scc1 .Lg_flush6
.Lg_cont6:
	v_cvt_f64_f32_e32 v[208:209], v90
	v_cvt_f64_f32_e32 v[210:211], v91
	v_cvt_f64_f32_e32 v[212:213], v92
	v_cvt_f64_f32_e32 v[214:215], v93
	v_add_f64 v[200:201], v[200:201], v[208:209]
	v_add_f64 v[202:203], v[202:203], v[210:211]
	v_add_f64 v[204:205], v[204:205], v[212:213]
	v_add_f64 v[206:207], v[206:207], v[214:215]
	s_add_u32 s41, s44, 24
	s_cmp_lt_u32 s41, s39
	s_cbranch_scc0 .Lg_tail6
	s_and_b32 s46, s41, 63
	v_readlane_b32 s40, v216, s46
	v_readlane_b32 s47, v217, s46
	s_cmp_lt_u32 s41, 64
	s_cselect_b32 s40, s40, s47
	s_bfe_u32 s66, s40, 0x40002
	s_and_b32 s40, s40, 0xffffffc0
	s_lshl_b32 s40, s40, 4
	s_add_u32 s42, s32, s40
	s_addc_u32 s43, s33, 0
	global_load_dwordx4 v[90:93], v218, s[42:43] nt

.Lg_slot7:
	s_waitcnt vmcnt(23)
	s_cmp_lg_u32 s67, s50
	s_cbranch_scc1 .Lg_flush7
.Lg_cont7:
	v_cvt_f64_f32_e32 v[208:209], v94
	v_cvt_f64_f32_e32 v[210:211], v95
	v_cvt_f64_f32_e32 v[212:213], v96
	v_cvt_f64_f32_e32 v[214:215], v97
	v_add_f64 v[200:201], v[200:201], v[208:209]
	v_add_f64 v[202:203], v[202:203], v[210:211]
	v_add_f64 v[204:205], v[204:205], v[212:213]
	v_add_f64 v[206:207], v[206:207], v[214:215]
	s_add_u32 s41, s44, 24
	s_cmp_lt_u32 s41, s39
	s_cbranch_scc0 .Lg_tail7
	s_and_b32 s46, s41, 63
	v_readlane_b32 s40, v216, s46
	v_readlane_b32 s47, v217, s46
	s_cmp_lt_u32 s41, 64
	s_cselect_b32 s40, s40, s47
	s_bfe_u32 s67, s40, 0x40002
	s_and_b32 s40, s40, 0xffffffc0
	s_lshl_b32 s40, s40, 4
	s_add_u32 s42, s32, s40
	s_addc_u32 s43, s33, 0
	global_load_dwordx4 v[94:97], v218, s[42:43] nt

.Lg_slot8:
	s_waitcnt vmcnt(23)
	s_cmp_lg_u32 s68, s50
	s_cbranch_scc1 .Lg_flush8
.Lg_cont8:
	v_cvt_f64_f32_e32 v[208:209], v98
	v_cvt_f64_f32_e32 v[210:211], v99
	v_cvt_f64_f32_e32 v[212:213], v100
	v_cvt_f64_f32_e32 v[214:215], v101
	v_add_f64 v[200:201], v[200:201], v[208:209]
	v_add_f64 v[202:203], v[202:203], v[210:211]
	v_add_f64 v[204:205], v[204:205], v[212:213]
	v_add_f64 v[206:207], v[206:207], v[214:215]
	s_add_u32 s41, s44, 24
	s_cmp_lt_u32 s41, s39
	s_cbranch_scc0 .Lg_tail8
	s_and_b32 s46, s41, 63
	v_readlane_b32 s40, v216, s46
	v_readlane_b32 s47, v217, s46
	s_cmp_lt_u32 s41, 64
	s_cselect_b32 s40, s40, s47
	s_bfe_u32 s68, s40, 0x40002
	s_and_b32 s40, s40, 0xffffffc0
	s_lshl_b32 s40, s40, 4
	s_add_u32 s42, s32, s40
	s_addc_u32 s43, s33, 0
	global_load_dwordx4 v[98:101], v218, s[42:43] nt

.Lg_slot9:
	s_waitcnt vmcnt(23)
	s_cmp_lg_u32 s69, s50
	s_cbranch_scc1 .Lg_flush9
.Lg_cont9:
	v_cvt_f64_f32_e32 v[208:209], v102
	v_cvt_f64_f32_e32 v[210:211], v103
	v_cvt_f64_f32_e32 v[212:213], v104
	v_cvt_f64_f32_e32 v[214:215], v105
	v_add_f64 v[200:201], v[200:201], v[208:209]
	v_add_f64 v[202:203], v[202:203], v[210:211]
	v_add_f64 v[204:205], v[204:205], v[212:213]
	v_add_f64 v[206:207], v[206:207], v[214:215]
	s_add_u32 s41, s44, 24
	s_cmp_lt_u32 s41, s39
	s_cbranch_scc0 .Lg_tail9
	s_and_b32 s46, s41, 63
	v_readlane_b32 s40, v216, s46
	v_readlane_b32 s47, v217, s46
	s_cmp_lt_u32 s41, 64
	s_cselect_b32 s40, s40, s47
	s_bfe_u32 s69, s40, 0x40002
	s_and_b32 s40, s40, 0xffffffc0
	s_lshl_b32 s40, s40, 4
	s_add_u32 s42, s32, s40
	s_addc_u32 s43, s33, 0
	global_load_dwordx4 v[102:105], v218, s[42:43] nt

.Lg_slot10:
	s_waitcnt vmcnt(23)
	s_cmp_lg_u32 s70, s50
	s_cbranch_scc1 .Lg_flush10
.Lg_cont10:
	v_cvt_f64_f32_e32 v[208:209], v106
	v_cvt_f64_f32_e32 v[210:211], v107
	v_cvt_f64_f32_e32 v[212:213], v108
	v_cvt_f64_f32_e32 v[214:215], v109
	v_add_f64 v[200:201], v[200:201], v[208:209]
	v_add_f64 v[202:203], v[202:203], v[210:211]
	v_add_f64 v[204:205], v[204:205], v[212:213]
	v_add_f64 v[206:207], v[206:207], v[214:215]
	s_add_u32 s41, s44, 24
	s_cmp_lt_u32 s41, s39
	s_cbranch_scc0 .Lg_tail10
	s_and_b32 s46, s41, 63
	v_readlane_b32 s40, v216, s46
	v_readlane_b32 s47, v217, s46
	s_cmp_lt_u32 s41, 64
	s_cselect_b32 s40, s40, s47
	s_bfe_u32 s70, s40, 0x40002
	s_and_b32 s40, s40, 0xffffffc0
	s_lshl_b32 s40, s40, 4
	s_add_u32 s42, s32, s40
	s_addc_u32 s43, s33, 0
	global_load_dwordx4 v[106:109], v218, s[42:43] nt

.Lg_slot11:
	s_waitcnt vmcnt(23)
	s_cmp_lg_u32 s71, s50
	s_cbranch_scc1 .Lg_flush11
.Lg_cont11:
	v_cvt_f64_f32_e32 v[208:209], v110
	v_cvt_f64_f32_e32 v[210:211], v111
	v_cvt_f64_f32_e32 v[212:213], v112
	v_cvt_f64_f32_e32 v[214:215], v113
	v_add_f64 v[200:201], v[200:201], v[208:209]
	v_add_f64 v[202:203], v[202:203], v[210:211]
	v_add_f64 v[204:205], v[204:205], v[212:213]
	v_add_f64 v[206:207], v[206:207], v[214:215]
	s_add_u32 s41, s44, 24
	s_cmp_lt_u32 s41, s39
	s_cbranch_scc0 .Lg_tail11
	s_and_b32 s46, s41, 63
	v_readlane_b32 s40, v216, s46
	v_readlane_b32 s47, v217, s46
	s_cmp_lt_u32 s41, 64
	s_cselect_b32 s40, s40, s47
	s_bfe_u32 s71, s40, 0x40002
	s_and_b32 s40, s40, 0xffffffc0
	s_lshl_b32 s40, s40, 4
	s_add_u32 s42, s32, s40
	s_addc_u32 s43, s33, 0
	global_load_dwordx4 v[110:113], v218, s[42:43] nt

.Lg_slot12:
	s_waitcnt vmcnt(23)
	s_cmp_lg_u32 s72, s50
	s_cbranch_scc1 .Lg_flush12
.Lg_cont12:
	v_cvt_f64_f32_e32 v[208:209], v114
	v_cvt_f64_f32_e32 v[210:211], v115
	v_cvt_f64_f32_e32 v[212:213], v116
	v_cvt_f64_f32_e32 v[214:215], v117
	v_add_f64 v[200:201], v[200:201], v[208:209]
	v_add_f64 v[202:203], v[202:203], v[210:211]
	v_add_f64 v[204:205], v[204:205], v[212:213]
	v_add_f64 v[206:207], v[206:207], v[214:215]
	s_add_u32 s41, s44, 24
	s_cmp_lt_u32 s41, s39
	s_cbranch_scc0 .Lg_tail12
	s_and_b32 s46, s41, 63
	v_readlane_b32 s40, v216, s46
	v_readlane_b32 s47, v217, s46
	s_cmp_lt_u32 s41, 64
	s_cselect_b32 s40, s40, s47
	s_bfe_u32 s72, s40, 0x40002
	s_and_b32 s40, s40, 0xffffffc0
	s_lshl_b32 s40, s40, 4
	s_add_u32 s42, s32, s40
	s_addc_u32 s43, s33, 0
	global_load_dwordx4 v[114:117], v218, s[42:43] nt

.Lg_slot13:
	s_waitcnt vmcnt(23)
	s_cmp_lg_u32 s73, s50
	s_cbranch_scc1 .Lg_flush13
.Lg_cont13:
	v_cvt_f64_f32_e32 v[208:209], v118
	v_cvt_f64_f32_e32 v[210:211], v119
	v_cvt_f64_f32_e32 v[212:213], v120
	v_cvt_f64_f32_e32 v[214:215], v121
	v_add_f64 v[200:201], v[200:201], v[208:209]
	v_add_f64 v[202:203], v[202:203], v[210:211]
	v_add_f64 v[204:205], v[204:205], v[212:213]
	v_add_f64 v[206:207], v[206:207], v[214:215]
	s_add_u32 s41, s44, 24
	s_cmp_lt_u32 s41, s39
	s_cbranch_scc0 .Lg_tail13
	s_and_b32 s46, s41, 63
	v_readlane_b32 s40, v216, s46
	v_readlane_b32 s47, v217, s46
	s_cmp_lt_u32 s41, 64
	s_cselect_b32 s40, s40, s47
	s_bfe_u32 s73, s40, 0x40002
	s_and_b32 s40, s40, 0xffffffc0
	s_lshl_b32 s40, s40, 4
	s_add_u32 s42, s32, s40
	s_addc_u32 s43, s33, 0
	global_load_dwordx4 v[118:121], v218, s[42:43] nt

.Lg_slot14:
	s_waitcnt vmcnt(23)
	s_cmp_lg_u32 s74, s50
	s_cbranch_scc1 .Lg_flush14
.Lg_cont14:
	v_cvt_f64_f32_e32 v[208:209], v122
	v_cvt_f64_f32_e32 v[210:211], v123
	v_cvt_f64_f32_e32 v[212:213], v124
	v_cvt_f64_f32_e32 v[214:215], v125
	v_add_f64 v[200:201], v[200:201], v[208:209]
	v_add_f64 v[202:203], v[202:203], v[210:211]
	v_add_f64 v[204:205], v[204:205], v[212:213]
	v_add_f64 v[206:207], v[206:207], v[214:215]
	s_add_u32 s41, s44, 24
	s_cmp_lt_u32 s41, s39
	s_cbranch_scc0 .Lg_tail14
	s_and_b32 s46, s41, 63
	v_readlane_b32 s40, v216, s46
	v_readlane_b32 s47, v217, s46
	s_cmp_lt_u32 s41, 64
	s_cselect_b32 s40, s40, s47
	s_bfe_u32 s74, s40, 0x40002
	s_and_b32 s40, s40, 0xffffffc0
	s_lshl_b32 s40, s40, 4
	s_add_u32 s42, s32, s40
	s_addc_u32 s43, s33, 0
	global_load_dwordx4 v[122:125], v218, s[42:43] nt

.Lg_slot15:
	s_waitcnt vmcnt(23)
	s_cmp_lg_u32 s75, s50
	s_cbranch_scc1 .Lg_flush15
.Lg_cont15:
	v_cvt_f64_f32_e32 v[208:209], v126
	v_cvt_f64_f32_e32 v[210:211], v127
	v_cvt_f64_f32_e32 v[212:213], v128
	v_cvt_f64_f32_e32 v[214:215], v129
	v_add_f64 v[200:201], v[200:201], v[208:209]
	v_add_f64 v[202:203], v[202:203], v[210:211]
	v_add_f64 v[204:205], v[204:205], v[212:213]
	v_add_f64 v[206:207], v[206:207], v[214:215]
	s_add_u32 s41, s44, 24
	s_cmp_lt_u32 s41, s39
	s_cbranch_scc0 .Lg_tail15
	s_and_b32 s46, s41, 63
	v_readlane_b32 s40, v216, s46
	v_readlane_b32 s47, v217, s46
	s_cmp_lt_u32 s41, 64
	s_cselect_b32 s40, s40, s47
	s_bfe_u32 s75, s40, 0x40002
	s_and_b32 s40, s40, 0xffffffc0
	s_lshl_b32 s40, s40, 4
	s_add_u32 s42, s32, s40
	s_addc_u32 s43, s33, 0
	global_load_dwordx4 v[126:129], v218, s[42:43] nt

.Lg_slot16:
	s_waitcnt vmcnt(23)
	s_cmp_lg_u32 s76, s50
	s_cbranch_scc1 .Lg_flush16
.Lg_cont16:
	v_cvt_f64_f32_e32 v[208:209], v130
	v_cvt_f64_f32_e32 v[210:211], v131
	v_cvt_f64_f32_e32 v[212:213], v132
	v_cvt_f64_f32_e32 v[214:215], v133
	v_add_f64 v[200:201], v[200:201], v[208:209]
	v_add_f64 v[202:203], v[202:203], v[210:211]
	v_add_f64 v[204:205], v[204:205], v[212:213]
	v_add_f64 v[206:207], v[206:207], v[214:215]
	s_add_u32 s41, s44, 24
	s_cmp_lt_u32 s41, s39
	s_cbranch_scc0 .Lg_tail16
	s_and_b32 s46, s41, 63
	v_readlane_b32 s40, v216, s46
	v_readlane_b32 s47, v217, s46
	s_cmp_lt_u32 s41, 64
	s_cselect_b32 s40, s40, s47
	s_bfe_u32 s76, s40, 0x40002
	s_and_b32 s40, s40, 0xffffffc0
	s_lshl_b32 s40, s40, 4
	s_add_u32 s42, s32, s40
	s_addc_u32 s43, s33, 0
	global_load_dwordx4 v[130:133], v218, s[42:43] nt

.Lg_slot17:
	s_waitcnt vmcnt(23)
	s_cmp_lg_u32 s77, s50
	s_cbranch_scc1 .Lg_flush17
.Lg_cont17:
	v_cvt_f64_f32_e32 v[208:209], v134
	v_cvt_f64_f32_e32 v[210:211], v135
	v_cvt_f64_f32_e32 v[212:213], v136
	v_cvt_f64_f32_e32 v[214:215], v137
	v_add_f64 v[200:201], v[200:201], v[208:209]
	v_add_f64 v[202:203], v[202:203], v[210:211]
	v_add_f64 v[204:205], v[204:205], v[212:213]
	v_add_f64 v[206:207], v[206:207], v[214:215]
	s_add_u32 s41, s44, 24
	s_cmp_lt_u32 s41, s39
	s_cbranch_scc0 .Lg_tail17
	s_and_b32 s46, s41, 63
	v_readlane_b32 s40, v216, s46
	v_readlane_b32 s47, v217, s46
	s_cmp_lt_u32 s41, 64
	s_cselect_b32 s40, s40, s47
	s_bfe_u32 s77, s40, 0x40002
	s_and_b32 s40, s40, 0xffffffc0
	s_lshl_b32 s40, s40, 4
	s_add_u32 s42, s32, s40
	s_addc_u32 s43, s33, 0
	global_load_dwordx4 v[134:137], v218, s[42:43] nt

.Lg_slot18:
	s_waitcnt vmcnt(23)
	s_cmp_lg_u32 s78, s50
	s_cbranch_scc1 .Lg_flush18
.Lg_cont18:
	v_cvt_f64_f32_e32 v[208:209], v138
	v_cvt_f64_f32_e32 v[210:211], v139
	v_cvt_f64_f32_e32 v[212:213], v140
	v_cvt_f64_f32_e32 v[214:215], v141
	v_add_f64 v[200:201], v[200:201], v[208:209]
	v_add_f64 v[202:203], v[202:203], v[210:211]
	v_add_f64 v[204:205], v[204:205], v[212:213]
	v_add_f64 v[206:207], v[206:207], v[214:215]
	s_add_u32 s41, s44, 24
	s_cmp_lt_u32 s41, s39
	s_cbranch_scc0 .Lg_tail18
	s_and_b32 s46, s41, 63
	v_readlane_b32 s40, v216, s46
	v_readlane_b32 s47, v217, s46
	s_cmp_lt_u32 s41, 64
	s_cselect_b32 s40, s40, s47
	s_bfe_u32 s78, s40, 0x40002
	s_and_b32 s40, s40, 0xffffffc0
	s_lshl_b32 s40, s40, 4
	s_add_u32 s42, s32, s40
	s_addc_u32 s43, s33, 0
	global_load_dwordx4 v[138:141], v218, s[42:43] nt

.Lg_slot19:
	s_waitcnt vmcnt(23)
	s_cmp_lg_u32 s79, s50
	s_cbranch_scc1 .Lg_flush19
.Lg_cont19:
	v_cvt_f64_f32_e32 v[208:209], v142
	v_cvt_f64_f32_e32 v[210:211], v143
	v_cvt_f64_f32_e32 v[212:213], v144
	v_cvt_f64_f32_e32 v[214:215], v145
	v_add_f64 v[200:201], v[200:201], v[208:209]
	v_add_f64 v[202:203], v[202:203], v[210:211]
	v_add_f64 v[204:205], v[204:205], v[212:213]
	v_add_f64 v[206:207], v[206:207], v[214:215]
	s_add_u32 s41, s44, 24
	s_cmp_lt_u32 s41, s39
	s_cbranch_scc0 .Lg_tail19
	s_and_b32 s46, s41, 63
	v_readlane_b32 s40, v216, s46
	v_readlane_b32 s47, v217, s46
	s_cmp_lt_u32 s41, 64
	s_cselect_b32 s40, s40, s47
	s_bfe_u32 s79, s40, 0x40002
	s_and_b32 s40, s40, 0xffffffc0
	s_lshl_b32 s40, s40, 4
	s_add_u32 s42, s32, s40
	s_addc_u32 s43, s33, 0
	global_load_dwordx4 v[142:145], v218, s[42:43] nt

.Lg_slot20:
	s_waitcnt vmcnt(23)
	s_cmp_lg_u32 s80, s50
	s_cbranch_scc1 .Lg_flush20
.Lg_cont20:
	v_cvt_f64_f32_e32 v[208:209], v146
	v_cvt_f64_f32_e32 v[210:211], v147
	v_cvt_f64_f32_e32 v[212:213], v148
	v_cvt_f64_f32_e32 v[214:215], v149
	v_add_f64 v[200:201], v[200:201], v[208:209]
	v_add_f64 v[202:203], v[202:203], v[210:211]
	v_add_f64 v[204:205], v[204:205], v[212:213]
	v_add_f64 v[206:207], v[206:207], v[214:215]
	s_add_u32 s41, s44, 24
	s_cmp_lt_u32 s41, s39
	s_cbranch_scc0 .Lg_tail20
	s_and_b32 s46, s41, 63
	v_readlane_b32 s40, v216, s46
	v_readlane_b32 s47, v217, s46
	s_cmp_lt_u32 s41, 64
	s_cselect_b32 s40, s40, s47
	s_bfe_u32 s80, s40, 0x40002
	s_and_b32 s40, s40, 0xffffffc0
	s_lshl_b32 s40, s40, 4
	s_add_u32 s42, s32, s40
	s_addc_u32 s43, s33, 0
	global_load_dwordx4 v[146:149], v218, s[42:43] nt

.Lg_slot21:
	s_waitcnt vmcnt(23)
	s_cmp_lg_u32 s81, s50
	s_cbranch_scc1 .Lg_flush21
.Lg_cont21:
	v_cvt_f64_f32_e32 v[208:209], v150
	v_cvt_f64_f32_e32 v[210:211], v151
	v_cvt_f64_f32_e32 v[212:213], v152
	v_cvt_f64_f32_e32 v[214:215], v153
	v_add_f64 v[200:201], v[200:201], v[208:209]
	v_add_f64 v[202:203], v[202:203], v[210:211]
	v_add_f64 v[204:205], v[204:205], v[212:213]
	v_add_f64 v[206:207], v[206:207], v[214:215]
	s_add_u32 s41, s44, 24
	s_cmp_lt_u32 s41, s39
	s_cbranch_scc0 .Lg_tail21
	s_and_b32 s46, s41, 63
	v_readlane_b32 s40, v216, s46
	v_readlane_b32 s47, v217, s46
	s_cmp_lt_u32 s41, 64
	s_cselect_b32 s40, s40, s47
	s_bfe_u32 s81, s40, 0x40002
	s_and_b32 s40, s40, 0xffffffc0
	s_lshl_b32 s40, s40, 4
	s_add_u32 s42, s32, s40
	s_addc_u32 s43, s33, 0
	global_load_dwordx4 v[150:153], v218, s[42:43] nt

.Lg_slot22:
	s_waitcnt vmcnt(23)
	s_cmp_lg_u32 s82, s50
	s_cbranch_scc1 .Lg_flush22
.Lg_cont22:
	v_cvt_f64_f32_e32 v[208:209], v154
	v_cvt_f64_f32_e32 v[210:211], v155
	v_cvt_f64_f32_e32 v[212:213], v156
	v_cvt_f64_f32_e32 v[214:215], v157
	v_add_f64 v[200:201], v[200:201], v[208:209]
	v_add_f64 v[202:203], v[202:203], v[210:211]
	v_add_f64 v[204:205], v[204:205], v[212:213]
	v_add_f64 v[206:207], v[206:207], v[214:215]
	s_add_u32 s41, s44, 24
	s_cmp_lt_u32 s41, s39
	s_cbranch_scc0 .Lg_tail22
	s_and_b32 s46, s41, 63
	v_readlane_b32 s40, v216, s46
	v_readlane_b32 s47, v217, s46
	s_cmp_lt_u32 s41, 64
	s_cselect_b32 s40, s40, s47
	s_bfe_u32 s82, s40, 0x40002
	s_and_b32 s40, s40, 0xffffffc0
	s_lshl_b32 s40, s40, 4
	s_add_u32 s42, s32, s40
	s_addc_u32 s43, s33, 0
	global_load_dwordx4 v[154:157], v218, s[42:43] nt

.Lg_slot23:
	s_waitcnt vmcnt(23)
	s_cmp_lg_u32 s83, s50
	s_cbranch_scc1 .Lg_flush23
.Lg_cont23:
	v_cvt_f64_f32_e32 v[208:209], v158
	v_cvt_f64_f32_e32 v[210:211], v159
	v_cvt_f64_f32_e32 v[212:213], v160
	v_cvt_f64_f32_e32 v[214:215], v161
	v_add_f64 v[200:201], v[200:201], v[208:209]
	v_add_f64 v[202:203], v[202:203], v[210:211]
	v_add_f64 v[204:205], v[204:205], v[212:213]
	v_add_f64 v[206:207], v[206:207], v[214:215]
	s_add_u32 s41, s44, 24
	s_cmp_lt_u32 s41, s39
	s_cbranch_scc0 .Lg_tail23
	s_and_b32 s46, s41, 63
	v_readlane_b32 s40, v216, s46
	v_readlane_b32 s47, v217, s46
	s_cmp_lt_u32 s41, 64
	s_cselect_b32 s40, s40, s47
	s_bfe_u32 s83, s40, 0x40002
	s_and_b32 s40, s40, 0xffffffc0
	s_lshl_b32 s40, s40, 4
	s_add_u32 s42, s32, s40
	s_addc_u32 s43, s33, 0
	global_load_dwordx4 v[158:161], v218, s[42:43] nt
.Lg_next23:
	s_add_u32 s44, s44, 1
	s_cmp_lt_u32 s44, s39
	s_cbranch_scc0 .Lg_blockdone
	s_branch .Lg_slot0
.Lg_tail0:
	s_waitcnt vmcnt(0)
	s_branch .Lg_next0

.Lg_flush0:
	s_mul_i32 s42, s50, 0x810
	v_add_u32_e32 v220, s42, v219
	ds_add_f64 v220, v[200:201] offset:32768
	ds_add_f64 v220, v[202:203] offset:33280
	ds_add_f64 v220, v[204:205] offset:33792
	ds_add_f64 v220, v[206:207] offset:34304
	v_mov_b32_e32 v200, 0
	v_mov_b32_e32 v201, 0
	v_mov_b32_e32 v202, 0
	v_mov_b32_e32 v203, 0
	v_mov_b32_e32 v204, 0
	v_mov_b32_e32 v205, 0
	v_mov_b32_e32 v206, 0
	v_mov_b32_e32 v207, 0
	s_mov_b32 s50, s60
	s_branch .Lg_cont0
.Lg_flush1:
	s_mul_i32 s42, s50, 0x810
	v_add_u32_e32 v220, s42, v219
	ds_add_f64 v220, v[200:201] offset:32768
	ds_add_f64 v220, v[202:203] offset:33280
	ds_add_f64 v220, v[204:205] offset:33792
	ds_add_f64 v220, v[206:207] offset:34304
	v_mov_b32_e32 v200, 0
	v_mov_b32_e32 v201, 0
	v_mov_b32_e32 v202, 0
	v_mov_b32_e32 v203, 0
	v_mov_b32_e32 v204, 0
	v_mov_b32_e32 v205, 0
	v_mov_b32_e32 v206, 0
	v_mov_b32_e32 v207, 0
	s_mov_b32 s50, s61
	s_branch .Lg_cont1
.Lg_flush2:
	s_mul_i32 s42, s50, 0x810
	v_add_u32_e32 v220, s42, v219
	ds_add_f64 v220, v[200:201] offset:32768
	ds_add_f64 v220, v[202:203] offset:33280
	ds_add_f64 v220, v[204:205] offset:33792
	ds_add_f64 v220, v[206:207] offset:34304
	v_mov_b32_e32 v200, 0
	v_mov_b32_e32 v201, 0
	v_mov_b32_e32 v202, 0
	v_mov_b32_e32 v203, 0
	v_mov_b32_e32 v204, 0
	v_mov_b32_e32 v205, 0
	v_mov_b32_e32 v206, 0
	v_mov_b32_e32 v207, 0
	s_mov_b32 s50, s62
	s_branch .Lg_cont2
.Lg_flush3:
	s_mul_i32 s42, s50, 0x810
	v_add_u32_e32 v220, s42, v219
	ds_add_f64 v220, v[200:201] offset:32768
	ds_add_f64 v220, v[202:203] offset:33280
	ds_add_f64 v220, v[204:205] offset:33792
	ds_add_f64 v220, v[206:207] offset:34304
	v_mov_b32_e32 v200, 0
	v_mov_b32_e32 v201, 0
	v_mov_b32_e32 v202, 0
	v_mov_b32_e32 v203, 0
	v_mov_b32_e32 v204, 0
	v_mov_b32_e32 v205, 0
	v_mov_b32_e32 v206, 0
	v_mov_b32_e32 v207, 0
	s_mov_b32 s50, s63
	s_branch .Lg_cont3
.Lg_flush4:
	s_mul_i32 s42, s50, 0x810
	v_add_u32_e32 v220, s42, v219
	ds_add_f64 v220, v[200:201] offset:32768
	ds_add_f64 v220, v[202:203] offset:33280
	ds_add_f64 v220, v[204:205] offset:33792
	ds_add_f64 v220, v[206:207] offset:34304
	v_mov_b32_e32 v200, 0
	v_mov_b32_e32 v201, 0
	v_mov_b32_e32 v202, 0
	v_mov_b32_e32 v203, 0
	v_mov_b32_e32 v204, 0
	v_mov_b32_e32 v205, 0
	v_mov_b32_e32 v206, 0
	v_mov_b32_e32 v207, 0
	s_mov_b32 s50, s64
	s_branch .Lg_cont4
.Lg_flush5:
	s_mul_i32 s42, s50, 0x810
	v_add_u32_e32 v220, s42, v219
	ds_add_f64 v220, v[200:201] offset:32768
	ds_add_f64 v220, v[202:203] offset:33280
	ds_add_f64 v220, v[204:205] offset:33792
	ds_add_f64 v220, v[206:207] offset:34304
	v_mov_b32_e32 v200, 0
	v_mov_b32_e32 v201, 0
	v_mov_b32_e32 v202, 0
	v_mov_b32_e32 v203, 0
	v_mov_b32_e32 v204, 0
	v_mov_b32_e32 v205, 0
	v_mov_b32_e32 v206, 0
	v_mov_b32_e32 v207, 0
	s_mov_b32 s50, s65
	s_branch .Lg_cont5
.Lg_flush6:
	s_mul_i32 s42, s50, 0x810
	v_add_u32_e32 v220, s42, v219
	ds_add_f64 v220, v[200:201] offset:32768
	ds_add_f64 v220, v[202:203] offset:33280
	ds_add_f64 v220, v[204:205] offset:33792
	ds_add_f64 v220, v[206:207] offset:34304
	v_mov_b32_e32 v200, 0
	v_mov_b32_e32 v201, 0
	v_mov_b32_e32 v202, 0
	v_mov_b32_e32 v203, 0
	v_mov_b32_e32 v204, 0
	v_mov_b32_e32 v205, 0
	v_mov_b32_e32 v206, 0
	v_mov_b32_e32 v207, 0
	s_mov_b32 s50, s66
	s_branch .Lg_cont6
.Lg_flush7:
	s_mul_i32 s42, s50, 0x810
	v_add_u32_e32 v220, s42, v219
	ds_add_f64 v220, v[200:201] offset:32768
	ds_add_f64 v220, v[202:203] offset:33280
	ds_add_f64 v220, v[204:205] offset:33792
	ds_add_f64 v220, v[206:207] offset:34304
	v_mov_b32_e32 v200, 0
	v_mov_b32_e32 v201, 0
	v_mov_b32_e32 v202, 0
	v_mov_b32_e32 v203, 0
	v_mov_b32_e32 v204, 0
	v_mov_b32_e32 v205, 0
	v_mov_b32_e32 v206, 0
	v_mov_b32_e32 v207, 0
	s_mov_b32 s50, s67
	s_branch .Lg_cont7
.Lg_flush8:
	s_mul_i32 s42, s50, 0x810
	v_add_u32_e32 v220, s42, v219
	ds_add_f64 v220, v[200:201] offset:32768
	ds_add_f64 v220, v[202:203] offset:33280
	ds_add_f64 v220, v[204:205] offset:33792
	ds_add_f64 v220, v[206:207] offset:34304
	v_mov_b32_e32 v200, 0
	v_mov_b32_e32 v201, 0
	v_mov_b32_e32 v202, 0
	v_mov_b32_e32 v203, 0
	v_mov_b32_e32 v204, 0
	v_mov_b32_e32 v205, 0
	v_mov_b32_e32 v206, 0
	v_mov_b32_e32 v207, 0
	s_mov_b32 s50, s68
	s_branch .Lg_cont8
.Lg_flush9:
	s_mul_i32 s42, s50, 0x810
	v_add_u32_e32 v220, s42, v219
	ds_add_f64 v220, v[200:201] offset:32768
	ds_add_f64 v220, v[202:203] offset:33280
	ds_add_f64 v220, v[204:205] offset:33792
	ds_add_f64 v220, v[206:207] offset:34304
	v_mov_b32_e32 v200, 0
	v_mov_b32_e32 v201, 0
	v_mov_b32_e32 v202, 0
	v_mov_b32_e32 v203, 0
	v_mov_b32_e32 v204, 0
	v_mov_b32_e32 v205, 0
	v_mov_b32_e32 v206, 0
	v_mov_b32_e32 v207, 0
	s_mov_b32 s50, s69
	s_branch .Lg_cont9
.Lg_flush10:
	s_mul_i32 s42, s50, 0x810
	v_add_u32_e32 v220, s42, v219
	ds_add_f64 v220, v[200:201] offset:32768
	ds_add_f64 v220, v[202:203] offset:33280
	ds_add_f64 v220, v[204:205] offset:33792
	ds_add_f64 v220, v[206:207] offset:34304
	v_mov_b32_e32 v200, 0
	v_mov_b32_e32 v201, 0
	v_mov_b32_e32 v202, 0
	v_mov_b32_e32 v203, 0
	v_mov_b32_e32 v204, 0
	v_mov_b32_e32 v205, 0
	v_mov_b32_e32 v206, 0
	v_mov_b32_e32 v207, 0
	s_mov_b32 s50, s70
	s_branch .Lg_cont10
.Lg_flush11:
	s_mul_i32 s42, s50, 0x810
	v_add_u32_e32 v220, s42, v219
	ds_add_f64 v220, v[200:201] offset:32768
	ds_add_f64 v220, v[202:203] offset:33280
	ds_add_f64 v220, v[204:205] offset:33792
	ds_add_f64 v220, v[206:207] offset:34304
	v_mov_b32_e32 v200, 0
	v_mov_b32_e32 v201, 0
	v_mov_b32_e32 v202, 0
	v_mov_b32_e32 v203, 0
	v_mov_b32_e32 v204, 0
	v_mov_b32_e32 v205, 0
	v_mov_b32_e32 v206, 0
	v_mov_b32_e32 v207, 0
	s_mov_b32 s50, s71
	s_branch .Lg_cont11
.Lg_flush12:
	s_mul_i32 s42, s50, 0x810
	v_add_u32_e32 v220, s42, v219
	ds_add_f64 v220, v[200:201] offset:32768
	ds_add_f64 v220, v[202:203] offset:33280
	ds_add_f64 v220, v[204:205] offset:33792
	ds_add_f64 v220, v[206:207] offset:34304
	v_mov_b32_e32 v200, 0
	v_mov_b32_e32 v201, 0
	v_mov_b32_e32 v202, 0
	v_mov_b32_e32 v203, 0
	v_mov_b32_e32 v204, 0
	v_mov_b32_e32 v205, 0
	v_mov_b32_e32 v206, 0
	v_mov_b32_e32 v207, 0
	s_mov_b32 s50, s72
	s_branch .Lg_cont12
.Lg_flush13:
	s_mul_i32 s42, s50, 0x810
	v_add_u32_e32 v220, s42, v219
	ds_add_f64 v220, v[200:201] offset:32768
	ds_add_f64 v220, v[202:203] offset:33280
	ds_add_f64 v220, v[204:205] offset:33792
	ds_add_f64 v220, v[206:207] offset:34304
	v_mov_b32_e32 v200, 0
	v_mov_b32_e32 v201, 0
	v_mov_b32_e32 v202, 0
	v_mov_b32_e32 v203, 0
	v_mov_b32_e32 v204, 0
	v_mov_b32_e32 v205, 0
	v_mov_b32_e32 v206, 0
	v_mov_b32_e32 v207, 0
	s_mov_b32 s50, s73
	s_branch .Lg_cont13
.Lg_flush14:
	s_mul_i32 s42, s50, 0x810
	v_add_u32_e32 v220, s42, v219
	ds_add_f64 v220, v[200:201] offset:32768
	ds_add_f64 v220, v[202:203] offset:33280
	ds_add_f64 v220, v[204:205] offset:33792
	ds_add_f64 v220, v[206:207] offset:34304
	v_mov_b32_e32 v200, 0
	v_mov_b32_e32 v201, 0
	v_mov_b32_e32 v202, 0
	v_mov_b32_e32 v203, 0
	v_mov_b32_e32 v204, 0
	v_mov_b32_e32 v205, 0
	v_mov_b32_e32 v206, 0
	v_mov_b32_e32 v207, 0
	s_mov_b32 s50, s74
	s_branch .Lg_cont14
.Lg_flush15:
	s_mul_i32 s42, s50, 0x810
	v_add_u32_e32 v220, s42, v219
	ds_add_f64 v220, v[200:201] offset:32768
	ds_add_f64 v220, v[202:203] offset:33280
	ds_add_f64 v220, v[204:205] offset:33792
	ds_add_f64 v220, v[206:207] offset:34304
	v_mov_b32_e32 v200, 0
	v_mov_b32_e32 v201, 0
	v_mov_b32_e32 v202, 0
	v_mov_b32_e32 v203, 0
	v_mov_b32_e32 v204, 0
	v_mov_b32_e32 v205, 0
	v_mov_b32_e32 v206, 0
	v_mov_b32_e32 v207, 0
	s_mov_b32 s50, s75
	s_branch .Lg_cont15
.Lg_flush16:
	s_mul_i32 s42, s50, 0x810
	v_add_u32_e32 v220, s42, v219
	ds_add_f64 v220, v[200:201] offset:32768
	ds_add_f64 v220, v[202:203] offset:33280
	ds_add_f64 v220, v[204:205] offset:33792
	ds_add_f64 v220, v[206:207] offset:34304
	v_mov_b32_e32 v200, 0
	v_mov_b32_e32 v201, 0
	v_mov_b32_e32 v202, 0
	v_mov_b32_e32 v203, 0
	v_mov_b32_e32 v204, 0
	v_mov_b32_e32 v205, 0
	v_mov_b32_e32 v206, 0
	v_mov_b32_e32 v207, 0
	s_mov_b32 s50, s76
	s_branch .Lg_cont16
.Lg_flush17:
	s_mul_i32 s42, s50, 0x810
	v_add_u32_e32 v220, s42, v219
	ds_add_f64 v220, v[200:201] offset:32768
	ds_add_f64 v220, v[202:203] offset:33280
	ds_add_f64 v220, v[204:205] offset:33792
	ds_add_f64 v220, v[206:207] offset:34304
	v_mov_b32_e32 v200, 0
	v_mov_b32_e32 v201, 0
	v_mov_b32_e32 v202, 0
	v_mov_b32_e32 v203, 0
	v_mov_b32_e32 v204, 0
	v_mov_b32_e32 v205, 0
	v_mov_b32_e32 v206, 0
	v_mov_b32_e32 v207, 0
	s_mov_b32 s50, s77
	s_branch .Lg_cont17
.Lg_flush18:
	s_mul_i32 s42, s50, 0x810
	v_add_u32_e32 v220, s42, v219
	ds_add_f64 v220, v[200:201] offset:32768
	ds_add_f64 v220, v[202:203] offset:33280
	ds_add_f64 v220, v[204:205] offset:33792
	ds_add_f64 v220, v[206:207] offset:34304
	v_mov_b32_e32 v200, 0
	v_mov_b32_e32 v201, 0
	v_mov_b32_e32 v202, 0
	v_mov_b32_e32 v203, 0
	v_mov_b32_e32 v204, 0
	v_mov_b32_e32 v205, 0
	v_mov_b32_e32 v206, 0
	v_mov_b32_e32 v207, 0
	s_mov_b32 s50, s78
	s_branch .Lg_cont18
.Lg_flush19:
	s_mul_i32 s42, s50, 0x810
	v_add_u32_e32 v220, s42, v219
	ds_add_f64 v220, v[200:201] offset:32768
	ds_add_f64 v220, v[202:203] offset:33280
	ds_add_f64 v220, v[204:205] offset:33792
	ds_add_f64 v220, v[206:207] offset:34304
	v_mov_b32_e32 v200, 0
	v_mov_b32_e32 v201, 0
	v_mov_b32_e32 v202, 0
	v_mov_b32_e32 v203, 0
	v_mov_b32_e32 v204, 0
	v_mov_b32_e32 v205, 0
	v_mov_b32_e32 v206, 0
	v_mov_b32_e32 v207, 0
	s_mov_b32 s50, s79
	s_branch .Lg_cont19
.Lg_flush20:
	s_mul_i32 s42, s50, 0x810
	v_add_u32_e32 v220, s42, v219
	ds_add_f64 v220, v[200:201] offset:32768
	ds_add_f64 v220, v[202:203] offset:33280
	ds_add_f64 v220, v[204:205] offset:33792
	ds_add_f64 v220, v[206:207] offset:34304
	v_mov_b32_e32 v200, 0
	v_mov_b32_e32 v201, 0
	v_mov_b32_e32 v202, 0
	v_mov_b32_e32 v203, 0
	v_mov_b32_e32 v204, 0
	v_mov_b32_e32 v205, 0
	v_mov_b32_e32 v206, 0
	v_mov_b32_e32 v207, 0
	s_mov_b32 s50, s80
	s_branch .Lg_cont20
.Lg_flush21:
	s_mul_i32 s42, s50, 0x810
	v_add_u32_e32 v220, s42, v219
	ds_add_f64 v220, v[200:201] offset:32768
	ds_add_f64 v220, v[202:203] offset:33280
	ds_add_f64 v220, v[204:205] offset:33792
	ds_add_f64 v220, v[206:207] offset:34304
	v_mov_b32_e32 v200, 0
	v_mov_b32_e32 v201, 0
	v_mov_b32_e32 v202, 0
	v_mov_b32_e32 v203, 0
	v_mov_b32_e32 v204, 0
	v_mov_b32_e32 v205, 0
	v_mov_b32_e32 v206, 0
	v_mov_b32_e32 v207, 0
	s_mov_b32 s50, s81
	s_branch .Lg_cont21
.Lg_flush22:
	s_mul_i32 s42, s50, 0x810
	v_add_u32_e32 v220, s42, v219
	ds_add_f64 v220, v[200:201] offset:32768
	ds_add_f64 v220, v[202:203] offset:33280
	ds_add_f64 v220, v[204:205] offset:33792
	ds_add_f64 v220, v[206:207] offset:34304
	v_mov_b32_e32 v200, 0
	v_mov_b32_e32 v201, 0
	v_mov_b32_e32 v202, 0
	v_mov_b32_e32 v203, 0
	v_mov_b32_e32 v204, 0
	v_mov_b32_e32 v205, 0
	v_mov_b32_e32 v206, 0
	v_mov_b32_e32 v207, 0
	s_mov_b32 s50, s82
	s_branch .Lg_cont22
.Lg_flush23:
	s_mul_i32 s42, s50, 0x810
	v_add_u32_e32 v220, s42, v219
	ds_add_f64 v220, v[200:201] offset:32768
	ds_add_f64 v220, v[202:203] offset:33280
	ds_add_f64 v220, v[204:205] offset:33792
	ds_add_f64 v220, v[206:207] offset:34304
	v_mov_b32_e32 v200, 0
	v_mov_b32_e32 v201, 0
	v_mov_b32_e32 v202, 0
	v_mov_b32_e32 v203, 0
	v_mov_b32_e32 v204, 0
	v_mov_b32_e32 v205, 0
	v_mov_b32_e32 v206, 0
	v_mov_b32_e32 v207, 0
	s_mov_b32 s50, s83
	s_branch .Lg_cont23
.Lg_blockdone:
	s_add_u32 s37, s37, s39
	s_cmp_lt_u32 s37, s38
	s_cbranch_scc1 .Lg_block
	s_mul_i32 s42, s50, 0x810
	v_add_u32_e32 v220, s42, v219
	ds_add_f64 v220, v[200:201] offset:32768
	ds_add_f64 v220, v[202:203] offset:33280
	ds_add_f64 v220, v[204:205] offset:33792
	ds_add_f64 v220, v[206:207] offset:34304
.Lg_alldone:
	v_and_b32_e32 v138, 15, v0
	v_or_b32_e32 v134, s24, v138
	v_lshlrev_b32_e32 v135, 3, v1
	v_lshlrev_b32_e32 v139, 2, v1
	v_bfe_u32 v140, v0, 4, 2
	v_cmp_eq_u32_e64 s[2:3], 0, v1

	.amdhsa_kernel _Z7vq_mainPKfPKiS0_PfPhPdPi
		.amdhsa_group_segment_fixed_size 71936
		.amdhsa_private_segment_fixed_size 0
		.amdhsa_kernarg_size 56
		.amdhsa_user_sgpr_count 2
		.amdhsa_user_sgpr_dispatch_ptr 0
		.amdhsa_user_sgpr_queue_ptr 0
		.amdhsa_user_sgpr_kernarg_segment_ptr 1
		.amdhsa_user_sgpr_dispatch_id 0
		.amdhsa_user_sgpr_kernarg_preload_length 0
		.amdhsa_user_sgpr_kernarg_preload_offset 0
		.amdhsa_user_sgpr_private_segment_size 0
		.amdhsa_uses_dynamic_stack 0
		.amdhsa_enable_private_segment 0
		.amdhsa_system_sgpr_workgroup_id_x 1
		.amdhsa_system_sgpr_workgroup_id_y 0
		.amdhsa_system_sgpr_workgroup_id_z 0
		.amdhsa_system_sgpr_workgroup_info 0
		.amdhsa_system_vgpr_workitem_id 0
		.amdhsa_next_free_vgpr 228
		.amdhsa_next_free_sgpr 102
		.amdhsa_accum_offset 224
		.amdhsa_reserve_vcc 1
		.amdhsa_float_round_mode_32 0
		.amdhsa_float_round_mode_16_64 0
		.amdhsa_float_denorm_mode_32 3
		.amdhsa_float_denorm_mode_16_64 3
		.amdhsa_dx10_clamp 1
		.amdhsa_ieee_mode 1
		.amdhsa_fp16_overflow 0
		.amdhsa_tg_split 0
		.amdhsa_exception_fp_ieee_invalid_op 0
		.amdhsa_exception_fp_denorm_src 0
		.amdhsa_exception_fp_ieee_div_zero 0
		.amdhsa_exception_fp_ieee_overflow 0
		.amdhsa_exception_fp_ieee_underflow 0
		.amdhsa_exception_fp_ieee_inexact 0
		.amdhsa_exception_int_div_zero 0
	.end_amdhsa_kernel

amdhsa.kernels:
  - .agpr_count:     4
    .args:
      - .actual_access:  read_only
        .address_space:  global
        .offset:         0
        .size:           8
        .value_kind:     global_buffer
      - .actual_access:  read_only
        .address_space:  global
        .offset:         8
        .size:           8
        .value_kind:     global_buffer
      - .actual_access:  read_only
        .address_space:  global
        .offset:         16
        .size:           8
        .value_kind:     global_buffer
      - .actual_access:  write_only
        .address_space:  global
        .offset:         24
        .size:           8
        .value_kind:     global_buffer
      - .actual_access:  write_only
        .address_space:  global
        .offset:         32
        .size:           8
        .value_kind:     global_buffer
      - .actual_access:  write_only
        .address_space:  global
        .offset:         40
        .size:           8
        .value_kind:     global_buffer
      - .actual_access:  write_only
        .address_space:  global
        .offset:         48
        .size:           8
        .value_kind:     global_buffer
    .group_segment_fixed_size: 71936
    .kernarg_segment_align: 8
    .kernarg_segment_size: 56
    .language:       OpenCL C
    .language_version:
      - 2
      - 0
    .max_flat_workgroup_size: 256
    .name:           _Z7vq_mainPKfPKiS0_PfPhPdPi
    .private_segment_fixed_size: 0
    .sgpr_count:     108
    .sgpr_spill_count: 0
    .symbol:         _Z7vq_mainPKfPKiS0_PfPhPdPi.kd
    .uniform_work_group_size: 1
    .uses_dynamic_stack: false
    .vgpr_count:     228
    .vgpr_spill_count: 0
    .wavefront_size: 64
  - .agpr_count:     0
    .args:
      - .actual_access:  read_only
        .address_space:  global
        .offset:         0
        .size:           8
        .value_kind:     global_buffer
      - .actual_access:  read_only
        .address_space:  global
        .offset:         8
        .size:           8
        .value_kind:     global_buffer
      - .actual_access:  read_only
        .address_space:  global
        .offset:         16
        .size:           8
        .value_kind:     global_buffer
      - .actual_access:  write_only
        .address_space:  global
        .offset:         24
        .size:           8
        .value_kind:     global_buffer
    .group_segment_fixed_size: 352
    .kernarg_segment_align: 8
    .kernarg_segment_size: 32
    .language:       OpenCL C
    .language_version:
      - 2
      - 0
    .max_flat_workgroup_size: 1024
    .name:           _Z11vq_finalizePK15HIP_vector_typeIjLj4EEPKdPKiPf
    .private_segment_fixed_size: 0
    .sgpr_count:     22
    .sgpr_spill_count: 0
    .symbol:         _Z11vq_finalizePK15HIP_vector_typeIjLj4EEPKdPKiPf.kd
    .uniform_work_group_size: 1
    .uses_dynamic_stack: false
    .vgpr_count:     24
    .vgpr_spill_count: 0
    .wavefront_size: 64
